# attention tile loop v8: one barrier per tile, waves 4-7 stream K/V by LDS-DMA two tiles ahead (4 K slots, 3 V buffers), each wave software-pipelines QK(t+1) with softmax-finish(t) and PV(t) with softm
# speedup vs baseline: 1.0164x; 1.0076x over previous
.LBB0_1088:
	v_lshlrev_b32_e32 v13, 3, v146
	v_and_b32_e32 v12, 0xc0, v12
	v_lshlrev_b32_e32 v14, 1, v146
	s_xor_b64 s[34:35], s[4:5], -1
	v_and_or_b32 v12, v13, 24, v12
	v_and_b32_e32 v14, 32, v14
	v_and_b32_e32 v13, 0x100, v13
	s_add_i32 s44, s44, s8
	v_or3_b32 v12, v12, v14, v13
	v_or_b32_e32 v13, s44, v145
	s_cmp_lg_u32 0, -1
	s_cselect_b32 s4, 0, 0
	s_lshr_b32 s46, s7, 6
	v_add_u32_e32 v163, 0xffffff91, v13
	v_lshlrev_b32_e32 v164, 4, v4
	v_lshlrev_b32_e32 v13, 4, v145
	s_add_i32 s38, 0, 0x10800
	s_add_i32 s47, s46, -2
	s_or_b32 s64, s44, 31
	v_and_b32_e32 v13, 0x70, v13
	v_add_u32_e32 v14, 32, v164
	v_lshl_add_u32 v171, v146, 2, s38
	s_lshl_b32 s38, s46, 8
	v_xad_u32 v168, v14, v13, 0
	v_add_u32_e32 v14, 64, v164
	s_add_u32 s38, s89, s38
	v_xad_u32 v169, v14, v13, 0
	v_add_u32_e32 v14, 0x60, v164
	s_addc_u32 s39, s88, 0
	s_and_b32 s7, s7, 0x1fc0
	s_add_i32 s6, s60, s6
	v_lshlrev_b32_e32 v144, 2, v4
	v_xad_u32 v166, v13, v164, 0
	v_xad_u32 v170, v14, v13, 0
	s_sub_i32 s65, s7, 64
	v_add_u32_e32 v13, s6, v145
	s_lshl_b32 s6, s46, 18
	v_ashrrev_i32_e32 v147, 31, v146
	v_sub_u32_e32 v13, v13, v144
	s_add_u32 s6, s90, s6
	v_lshl_add_u64 v[148:149], v[146:147], 2, s[38:39]
	v_subrev_u32_e32 v147, s7, v13
	s_addc_u32 s7, s91, 0
	v_add_u32_e32 v0, v0, v10
	v_lshl_add_u64 v[150:151], s[6:7], 0, v[0:1]
	v_add3_u32 v0, s61, v6, v11
	v_lshl_add_u64 v[152:153], s[6:7], 0, v[0:1]
	v_add_u32_e32 v0, v7, v5
	v_add3_u32 v0, v0, v8, v2
	v_lshl_or_b32 v0, v0, 12, v9
	v_add_u32_e32 v0, v0, v3
	v_lshl_add_u64 v[154:155], s[6:7], 0, v[0:1]
	v_add_u32_e32 v0, s62, v4
	v_lshlrev_b32_e32 v4, 1, v0
	s_mov_b32 s38, 0xffff0
	v_and_or_b32 v4, v4, s38, v5
	v_and_b32_e32 v0, 4, v0
	v_add_u32_e32 v162, s4, v12
	v_lshrrev_b32_e32 v12, 5, v146
	v_add_u32_e32 v0, v4, v0
	v_add_lshl_u32 v0, v0, v2, 12
	v_add_u16_e32 v2, 2, v12
	v_and_b32_e32 v2, 3, v2
	v_lshlrev_b32_e32 v2, 6, v2
	s_waitcnt vmcnt(0)
	v_or3_b32 v0, v0, v2, v3
	v_mov_b32_e32 v14, v1
	v_mov_b32_e32 v15, v1
	v_lshl_add_u64 v[156:157], s[6:7], 0, v[0:1]
	v_mov_b32_e32 v0, v1
	v_mov_b32_e32 v2, v1
	v_mov_b32_e32 v3, v1
	v_mov_b32_e32 v4, v1
	v_mov_b32_e32 v5, v1
	v_mov_b32_e32 v6, v1
	v_mov_b32_e32 v7, v1
	v_mov_b32_e32 v8, v1
	v_mov_b32_e32 v9, v1
	v_mov_b32_e32 v10, v1
	v_mov_b32_e32 v11, v1
	v_mov_b32_e32 v12, v1
	v_mov_b32_e32 v13, v1
	s_waitcnt lgkmcnt(0)
	v_mov_b64_e32 v[30:31], v[14:15]
	v_mov_b64_e32 v[46:47], v[14:15]
	v_mov_b64_e32 v[62:63], v[14:15]
	v_mov_b64_e32 v[78:79], v[14:15]
	s_mov_b32 s45, 0
	v_lshlrev_b32_e32 v165, 8, v145
	v_cmp_gt_u32_e64 s[4:5], 32, v146
	v_lshl_add_u32 v167, v145, 2, s54
	v_add_u32_e32 v161, s54, v164
	v_mov_b32_e32 v174, 0
	v_mov_b32_e32 v173, 0xf149f2ca
	s_mov_b32 s66, s46
	v_mov_b64_e32 v[28:29], v[12:13]
	v_mov_b64_e32 v[26:27], v[10:11]
	v_mov_b64_e32 v[24:25], v[8:9]
	v_mov_b64_e32 v[22:23], v[6:7]
	v_mov_b64_e32 v[20:21], v[4:5]
	v_mov_b64_e32 v[18:19], v[2:3]
	v_mov_b64_e32 v[16:17], v[0:1]
	v_mov_b64_e32 v[44:45], v[12:13]
	v_mov_b64_e32 v[42:43], v[10:11]
	v_mov_b64_e32 v[40:41], v[8:9]
	v_mov_b64_e32 v[38:39], v[6:7]
	v_mov_b64_e32 v[36:37], v[4:5]
	v_mov_b64_e32 v[34:35], v[2:3]
	v_mov_b64_e32 v[32:33], v[0:1]
	v_mov_b64_e32 v[60:61], v[12:13]
	v_mov_b64_e32 v[58:59], v[10:11]
	v_mov_b64_e32 v[56:57], v[8:9]
	v_mov_b64_e32 v[54:55], v[6:7]
	v_mov_b64_e32 v[52:53], v[4:5]
	v_mov_b64_e32 v[50:51], v[2:3]
	v_mov_b64_e32 v[48:49], v[0:1]
	v_mov_b64_e32 v[76:77], v[12:13]
	v_mov_b64_e32 v[74:75], v[10:11]
	v_mov_b64_e32 v[72:73], v[8:9]
	v_mov_b64_e32 v[70:71], v[6:7]
	v_mov_b64_e32 v[68:69], v[4:5]
	v_mov_b64_e32 v[66:67], v[2:3]
	v_mov_b64_e32 v[64:65], v[0:1]
	s_waitcnt vmcnt(0)
	s_barrier
	s_mov_b32 s45, 0
	s_lshl_b32 s65, s46, 6
	s_mov_b32 s66, 0
	s_mov_b32 s33, 0x8000
	s_mov_b32 s42, 0x11000
	s_mov_b32 s43, 0x15000
	s_mov_b32 s47, 0x19000
	s_mov_b32 s99, 0
	v_subrev_u32_e32 v147, 64, v147
	v_lshlrev_b32_e32 v232, 2, v146
	s_lshr_b32 s6, s68, 11
	s_and_b32 s7, s6, 3
	s_lshl_b32 s98, s7, 12
	s_lshl_b32 s7, s7, 16
	s_add_i32 s40, s46, -1
	s_lshl_b32 s41, s40, 8
	s_lshl_b32 s39, s40, 18
	s_add_u32 s40, s30, s41
	s_addc_u32 s41, s31, 0
	s_add_u32 s39, s39, s7
	s_cmp_ge_u32 s6, 4
	s_cbranch_scc0 .Lat_setup_done
	s_add_u32 s100, s82, s39
	s_addc_u32 s101, s83, 0
	s_add_u32 s38, s84, s39
	s_addc_u32 s39, s85, 0
	v_lshrrev_b32_e32 v0, 4, v146
	v_and_b32_e32 v2, 15, v146
	v_xor_b32_e32 v2, v2, v0
	v_lshlrev_b32_e32 v2, 4, v2
	v_lshl_add_u32 v14, v0, 12, v2
	v_xor_b32_e32 v15, 64, v14
	v_add_u32_e32 v15, 0x4000, v15
	v_add_u32_e32 v175, 0x8000, v14
	v_xor_b32_e32 v155, 64, v14
	v_add_u32_e32 v155, 0xc000, v155
	v_bfe_u32 v0, v146, 4, 1
	v_bfe_u32 v2, v146, 2, 2
	v_lshl_add_u32 v0, v0, 3, v2
	v_lshlrev_b32_e32 v0, 12, v0
	v_lshrrev_b32_e32 v2, 5, v146
	v_lshl_add_u32 v0, v2, 6, v0
	v_and_b32_e32 v2, 3, v146
	v_lshl_add_u32 v228, v2, 4, v0
	v_add_u32_e32 v229, 0x80, v228
	v_add_u32_e32 v230, 0x4000, v228
	v_add_u32_e32 v231, 0x4080, v228
	s_add_i32 s6, s98, 0x4000
	s_mov_b32 s7, s6
	s_mov_b32 m0, s7
	s_add_i32 s7, s7, 0x400
	global_load_lds_dwordx4 v228, s[38:39]
	s_mov_b32 m0, s7
	s_add_i32 s7, s7, 0x400
	global_load_lds_dwordx4 v229, s[38:39]
	s_mov_b32 m0, s7
	s_add_i32 s7, s7, 0x400
	global_load_lds_dwordx4 v230, s[38:39]
	s_mov_b32 m0, s7
	s_nop 0
	global_load_lds_dwordx4 v231, s[38:39]
	s_sub_u32 s38, s38, 0x40000
	s_subb_u32 s39, s39, 0
	s_add_i32 s6, s42, s98
	s_mov_b32 s7, s6
	s_mov_b32 m0, s7
	s_add_i32 s7, s7, 0x400
	global_load_lds_dwordx4 v14, s[100:101]
	s_mov_b32 m0, s7
	s_add_i32 s7, s7, 0x400
	global_load_lds_dwordx4 v15, s[100:101]
	s_mov_b32 m0, s7
	s_add_i32 s7, s7, 0x400
	global_load_lds_dwordx4 v175, s[100:101]
	s_mov_b32 m0, s7
	s_nop 0
	global_load_lds_dwordx4 v155, s[100:101]
	global_load_dword v154, v232, s[40:41]
	s_sub_u32 s100, s100, 0x40000
	s_subb_u32 s101, s101, 0
	s_sub_u32 s40, s40, 0x100
	s_subb_u32 s41, s41, 0
	s_add_i32 s6, s43, s98
	s_mov_b32 s7, s6
	s_mov_b32 m0, s7
	s_add_i32 s7, s7, 0x400
	global_load_lds_dwordx4 v14, s[100:101]
	s_mov_b32 m0, s7
	s_add_i32 s7, s7, 0x400
	global_load_lds_dwordx4 v15, s[100:101]
	s_mov_b32 m0, s7
	s_add_i32 s7, s7, 0x400
	global_load_lds_dwordx4 v175, s[100:101]
	s_mov_b32 m0, s7
	s_nop 0
	global_load_lds_dwordx4 v155, s[100:101]
	global_load_dword v172, v232, s[40:41]
	s_sub_u32 s100, s100, 0x40000
	s_subb_u32 s101, s101, 0
	s_sub_u32 s40, s40, 0x100
	s_subb_u32 s41, s41, 0
	s_add_i32 s6, s47, s98
	s_mov_b32 s7, s6
	s_mov_b32 m0, s7
	s_add_i32 s7, s7, 0x400
	global_load_lds_dwordx4 v14, s[100:101]
	s_mov_b32 m0, s7
	s_add_i32 s7, s7, 0x400
	global_load_lds_dwordx4 v15, s[100:101]
	s_mov_b32 m0, s7
	s_add_i32 s7, s7, 0x400
	global_load_lds_dwordx4 v175, s[100:101]
	s_mov_b32 m0, s7
	s_nop 0
	global_load_lds_dwordx4 v155, s[100:101]
	global_load_dword v156, v232, s[40:41]
	s_sub_u32 s100, s100, 0x40000
	s_subb_u32 s101, s101, 0
	s_sub_u32 s40, s40, 0x100
	s_subb_u32 s41, s41, 0
	s_waitcnt vmcnt(0)
	s_cmp_lg_u32 s68, 0x2000
	s_cbranch_scc1 .Lat_setup_done
	v_add_u32_e32 v0, 256, v171
	ds_write_b32 v0, v154
	v_add_u32_e32 v0, 512, v171
	ds_write_b32 v0, v172
	v_add_u32_e32 v0, 768, v171
	ds_write_b32 v0, v156
	s_waitcnt lgkmcnt(0)
.Lat_setup_done:
	s_barrier
	s_cmp_gt_i32 s65, s64
	s_cbranch_scc1 .Lat_tile0
	v_add3_u32 v246, v166, v165, s33
	v_add3_u32 v247, v168, v165, s33
	v_add3_u32 v248, v169, v165, s33
	v_add3_u32 v249, v170, v165, s33
	ds_read_b128 v[208:211], v246
	ds_read_b128 v[212:215], v246 offset:8192
	ds_read_b128 v[216:219], v247
	ds_read_b128 v[220:223], v247 offset:8192
	ds_read_b128 v[224:227], v248
	ds_read_b128 v[234:237], v248 offset:8192
	ds_read_b128 v[238:241], v249
	ds_read_b128 v[242:245], v249 offset:8192
	s_add_i32 s6, s45, 0
	s_and_b32 s6, s6, 3
	s_lshl_b32 s6, s6, 8
	s_add_i32 s6, s6, 0x10800
	v_add_u32_e32 v152, s6, v164
	ds_read_b128 v[96:99], v152
	ds_read_b128 v[100:103], v152 offset:32
	ds_read_b128 v[80:83], v152 offset:128
	ds_read_b128 v[84:87], v152 offset:160
	ds_read_b128 v[104:107], v152 offset:64
	ds_read_b128 v[108:111], v152 offset:96
	ds_read_b128 v[88:91], v152 offset:192
	ds_read_b128 v[92:95], v152 offset:224
	s_waitcnt lgkmcnt(0)
	v_mfma_f32_32x32x16_bf16 v[96:111], v[208:211], v[112:115], v[96:111]
	ds_read_b128 v[208:211], v246 offset:128
	v_mfma_f32_32x32x16_bf16 v[80:95], v[212:215], v[112:115], v[80:95]
	ds_read_b128 v[212:215], v246 offset:8320
	v_mfma_f32_32x32x16_bf16 v[96:111], v[216:219], v[116:119], v[96:111]
	ds_read_b128 v[216:219], v247 offset:128
	v_mfma_f32_32x32x16_bf16 v[80:95], v[220:223], v[116:119], v[80:95]
	ds_read_b128 v[220:223], v247 offset:8320
	v_mfma_f32_32x32x16_bf16 v[96:111], v[224:227], v[120:123], v[96:111]
	ds_read_b128 v[224:227], v248 offset:128
	v_mfma_f32_32x32x16_bf16 v[80:95], v[234:237], v[120:123], v[80:95]
	ds_read_b128 v[234:237], v248 offset:8320
	v_mfma_f32_32x32x16_bf16 v[96:111], v[238:241], v[124:127], v[96:111]
	ds_read_b128 v[238:241], v249 offset:128
	v_mfma_f32_32x32x16_bf16 v[80:95], v[242:245], v[124:127], v[80:95]
	ds_read_b128 v[242:245], v249 offset:8320
	s_waitcnt lgkmcnt(7)
	v_mfma_f32_32x32x16_bf16 v[96:111], v[208:211], v[128:131], v[96:111]
	v_add3_u32 v246, v166, v165, s42
	v_add3_u32 v247, v168, v165, s42
	v_add3_u32 v248, v169, v165, s42
	v_add3_u32 v249, v170, v165, s42
	ds_read_b128 v[208:211], v246
	s_waitcnt lgkmcnt(7)
	v_mfma_f32_32x32x16_bf16 v[80:95], v[212:215], v[128:131], v[80:95]
	ds_read_b128 v[212:215], v246 offset:8192
	s_waitcnt lgkmcnt(7)
	v_mfma_f32_32x32x16_bf16 v[96:111], v[216:219], v[132:135], v[96:111]
	ds_read_b128 v[216:219], v247
	s_waitcnt lgkmcnt(7)
	v_mfma_f32_32x32x16_bf16 v[80:95], v[220:223], v[132:135], v[80:95]
	ds_read_b128 v[220:223], v247 offset:8192
	s_waitcnt lgkmcnt(7)
	v_mfma_f32_32x32x16_bf16 v[96:111], v[224:227], v[136:139], v[96:111]
	ds_read_b128 v[224:227], v248
	s_waitcnt lgkmcnt(7)
	v_mfma_f32_32x32x16_bf16 v[80:95], v[234:237], v[136:139], v[80:95]
	ds_read_b128 v[234:237], v248 offset:8192
	s_waitcnt lgkmcnt(7)
	v_mfma_f32_32x32x16_bf16 v[96:111], v[238:241], v[140:143], v[96:111]
	ds_read_b128 v[238:241], v249
	s_waitcnt lgkmcnt(7)
	v_mfma_f32_32x32x16_bf16 v[80:95], v[242:245], v[140:143], v[80:95]
	ds_read_b128 v[242:245], v249 offset:8192
	s_add_i32 s6, s65, 63
	s_cmp_gt_i32 s6, s44
	s_cbranch_scc1 .Lat_pmasks
	s_cmp_lt_i32 s65, 0x70
	s_cbranch_scc0 .Lat_pnomasks

.Lat_pnomasks:
	s_nop 13
	v_max3_f32 v0, v96, v97, v98
	v_max3_f32 v2, v104, v105, v106
	v_max3_f32 v3, v80, v81, v82
	v_max3_f32 v4, v88, v89, v90
	v_max3_f32 v0, v0, v99, v100
	v_max3_f32 v2, v2, v107, v108
	v_max3_f32 v3, v3, v83, v84
	v_max3_f32 v4, v4, v91, v92
	v_max3_f32 v0, v0, v101, v102
	v_max3_f32 v2, v2, v109, v110
	v_max3_f32 v3, v3, v85, v86
	v_max3_f32 v4, v4, v93, v94
	v_max_f32_e32 v0, v0, v103
	v_max_f32_e32 v2, v2, v111
	v_max_f32_e32 v3, v3, v87
	v_max_f32_e32 v4, v4, v95
	v_max3_f32 v0, v0, v2, v3
	v_max_f32_e32 v0, v0, v4
	v_mov_b32_e32 v2, v0
	s_nop 1
	v_permlane32_swap_b32_e32 v0, v2
	v_max_f32_e32 v2, v2, v2
	v_max_f32_e32 v0, v0, v0
	v_max_f32_e32 v0, v0, v2
	v_sub_f32_e32 v2, v0, v173
	v_mul_f32_e32 v2, 0x3db504f3, v2
	v_cmp_ge_f32_e32 vcc, s63, v2
	v_max_f32_e32 v2, v173, v173
	v_max_f32_e32 v2, v2, v0
	v_sub_f32_e32 v0, v173, v2
	v_mul_f32_e32 v0, 0x3e0293ee, v0
	v_exp_f32_e32 v0, v0
	s_cmp_eq_u64 vcc, exec
	s_cselect_b64 s[6:7], -1, 0
	v_cndmask_b32_e64 v0, v0, 1.0, s[6:7]
	v_cmp_gt_f32_e32 vcc, 1.0, v0
	v_mov_b32_e32 v233, v0
	v_cndmask_b32_e64 v173, v2, v173, s[6:7]
	s_cmp_lg_u64 vcc, 0
	s_cselect_b32 s99, 1, 0
	v_mul_f32_e32 v2, 0xbe0293ee, v173
	v_fmamk_f32 v96, v96, 0x3e0293ee, v2
	v_fmamk_f32 v97, v97, 0x3e0293ee, v2
	v_fmamk_f32 v98, v98, 0x3e0293ee, v2
	v_fmamk_f32 v99, v99, 0x3e0293ee, v2
	v_fmamk_f32 v100, v100, 0x3e0293ee, v2
	v_fmamk_f32 v101, v101, 0x3e0293ee, v2
	v_fmamk_f32 v102, v102, 0x3e0293ee, v2
	v_fmamk_f32 v103, v103, 0x3e0293ee, v2
	v_fmamk_f32 v104, v104, 0x3e0293ee, v2
	v_fmamk_f32 v105, v105, 0x3e0293ee, v2
	v_fmamk_f32 v106, v106, 0x3e0293ee, v2
	v_fmamk_f32 v107, v107, 0x3e0293ee, v2
	v_fmamk_f32 v108, v108, 0x3e0293ee, v2
	v_fmamk_f32 v109, v109, 0x3e0293ee, v2
	v_fmamk_f32 v110, v110, 0x3e0293ee, v2
	v_fmamk_f32 v111, v111, 0x3e0293ee, v2
	v_exp_f32_e32 v96, v96
	v_fmamk_f32 v80, v80, 0x3e0293ee, v2
	v_exp_f32_e32 v97, v97
	v_fmamk_f32 v81, v81, 0x3e0293ee, v2
	v_exp_f32_e32 v98, v98
	v_fmamk_f32 v82, v82, 0x3e0293ee, v2
	v_exp_f32_e32 v99, v99
	v_fmamk_f32 v83, v83, 0x3e0293ee, v2
	v_exp_f32_e32 v100, v100
	v_fmamk_f32 v84, v84, 0x3e0293ee, v2
	v_exp_f32_e32 v101, v101
	v_fmamk_f32 v85, v85, 0x3e0293ee, v2
	v_exp_f32_e32 v102, v102
	v_fmamk_f32 v86, v86, 0x3e0293ee, v2
	v_exp_f32_e32 v103, v103
	v_fmamk_f32 v87, v87, 0x3e0293ee, v2
	v_exp_f32_e32 v104, v104
	v_fmamk_f32 v88, v88, 0x3e0293ee, v2
	v_exp_f32_e32 v105, v105
	v_fmamk_f32 v89, v89, 0x3e0293ee, v2
	v_exp_f32_e32 v106, v106
	v_fmamk_f32 v90, v90, 0x3e0293ee, v2
	v_exp_f32_e32 v107, v107
	v_fmamk_f32 v91, v91, 0x3e0293ee, v2
	v_exp_f32_e32 v108, v108
	v_fmamk_f32 v92, v92, 0x3e0293ee, v2
	v_exp_f32_e32 v109, v109
	v_fmamk_f32 v93, v93, 0x3e0293ee, v2
	v_exp_f32_e32 v110, v110
	v_fmamk_f32 v94, v94, 0x3e0293ee, v2
	v_exp_f32_e32 v111, v111
	v_fmamk_f32 v95, v95, 0x3e0293ee, v2
	s_add_i32 s6, s45, 1
	s_and_b32 s6, s6, 3
	s_lshl_b32 s6, s6, 8
	s_add_i32 s6, s6, 0x10800
	v_add_u32_e32 v152, s6, v164
	ds_read_b128 v[176:179], v152
	ds_read_b128 v[180:183], v152 offset:32
	ds_read_b128 v[192:195], v152 offset:128
	ds_read_b128 v[196:199], v152 offset:160
	ds_read_b128 v[184:187], v152 offset:64
	ds_read_b128 v[188:191], v152 offset:96
	ds_read_b128 v[200:203], v152 offset:192
	ds_read_b128 v[204:207], v152 offset:224
.Lat_tile0:
	s_waitcnt lgkmcnt(0)
	s_barrier
	s_cmp_ge_u32 s68, 0x2000
	s_cbranch_scc0 .Lat_go0
	s_add_i32 s6, s45, 2
	s_cmp_ge_u32 s6, s46
	s_cbranch_scc1 .Lat_go0
	s_cmp_eq_u32 s66, 0
	s_cselect_b32 s6, 0xc000, 0
	s_cmp_eq_u32 s66, 0xc000
	s_cselect_b32 s6, 0x4000, s6
	s_add_i32 s6, s6, s98
	s_mov_b32 s7, s6
	s_mov_b32 m0, s7
	s_add_i32 s7, s7, 0x400
	global_load_lds_dwordx4 v228, s[38:39]
	s_mov_b32 m0, s7
	s_add_i32 s7, s7, 0x400
	global_load_lds_dwordx4 v229, s[38:39]
	s_mov_b32 m0, s7
	s_add_i32 s7, s7, 0x400
	global_load_lds_dwordx4 v230, s[38:39]
	s_mov_b32 m0, s7
	s_nop 0
	global_load_lds_dwordx4 v231, s[38:39]
	s_add_i32 s6, s45, 4
	s_cmp_ge_u32 s6, s46
	s_cbranch_scc1 .Lat_go0
	s_add_i32 s6, s33, s98
	s_mov_b32 s7, s6
	s_mov_b32 m0, s7
	s_add_i32 s7, s7, 0x400
	global_load_lds_dwordx4 v14, s[100:101]
	s_mov_b32 m0, s7
	s_add_i32 s7, s7, 0x400
	global_load_lds_dwordx4 v15, s[100:101]
	s_mov_b32 m0, s7
	s_add_i32 s7, s7, 0x400
	global_load_lds_dwordx4 v175, s[100:101]
	s_mov_b32 m0, s7
	s_nop 0
	global_load_lds_dwordx4 v155, s[100:101]
	global_load_dword v172, v232, s[40:41]
.Lat_go0:
	s_cmp_gt_i32 s65, s64
	s_cbranch_scc0 .Lat_steady0
	s_add_i32 s6, s65, 0xffffffc0
	s_cmp_gt_i32 s6, s64
	s_cbranch_scc1 .Lat_turn_end0
	s_add_i32 s6, s45, 1
	s_cmp_ge_u32 s6, s46
	s_cbranch_scc1 .Lat_turn_end0
	v_add3_u32 v246, v166, v165, s42
	v_add3_u32 v247, v168, v165, s42
	v_add3_u32 v248, v169, v165, s42
	v_add3_u32 v249, v170, v165, s42
	ds_read_b128 v[208:211], v246
	ds_read_b128 v[212:215], v246 offset:8192
	ds_read_b128 v[216:219], v247
	ds_read_b128 v[220:223], v247 offset:8192
	ds_read_b128 v[224:227], v248
	ds_read_b128 v[234:237], v248 offset:8192
	ds_read_b128 v[238:241], v249
	ds_read_b128 v[242:245], v249 offset:8192
	s_add_i32 s6, s45, 1
	s_and_b32 s6, s6, 3
	s_lshl_b32 s6, s6, 8
	s_add_i32 s6, s6, 0x10800
	v_add_u32_e32 v152, s6, v164
	ds_read_b128 v[176:179], v152
	ds_read_b128 v[180:183], v152 offset:32
	ds_read_b128 v[192:195], v152 offset:128
	ds_read_b128 v[196:199], v152 offset:160
	ds_read_b128 v[184:187], v152 offset:64
	ds_read_b128 v[188:191], v152 offset:96
	ds_read_b128 v[200:203], v152 offset:192
	ds_read_b128 v[204:207], v152 offset:224
	s_waitcnt lgkmcnt(0)
	v_mfma_f32_32x32x16_bf16 v[176:191], v[208:211], v[112:115], v[176:191]
	ds_read_b128 v[208:211], v246 offset:128
	v_mfma_f32_32x32x16_bf16 v[192:207], v[212:215], v[112:115], v[192:207]
	ds_read_b128 v[212:215], v246 offset:8320
	v_mfma_f32_32x32x16_bf16 v[176:191], v[216:219], v[116:119], v[176:191]
	ds_read_b128 v[216:219], v247 offset:128
	v_mfma_f32_32x32x16_bf16 v[192:207], v[220:223], v[116:119], v[192:207]
	ds_read_b128 v[220:223], v247 offset:8320
	v_mfma_f32_32x32x16_bf16 v[176:191], v[224:227], v[120:123], v[176:191]
	ds_read_b128 v[224:227], v248 offset:128
	v_mfma_f32_32x32x16_bf16 v[192:207], v[234:237], v[120:123], v[192:207]
	ds_read_b128 v[234:237], v248 offset:8320
	v_mfma_f32_32x32x16_bf16 v[176:191], v[238:241], v[124:127], v[176:191]
	ds_read_b128 v[238:241], v249 offset:128
	v_mfma_f32_32x32x16_bf16 v[192:207], v[242:245], v[124:127], v[192:207]
	ds_read_b128 v[242:245], v249 offset:8320
	s_waitcnt lgkmcnt(7)
	v_mfma_f32_32x32x16_bf16 v[176:191], v[208:211], v[128:131], v[176:191]
	v_add3_u32 v246, v166, v165, s43
	v_add3_u32 v247, v168, v165, s43
	v_add3_u32 v248, v169, v165, s43
	v_add3_u32 v249, v170, v165, s43
	ds_read_b128 v[208:211], v246
	s_waitcnt lgkmcnt(7)
	v_mfma_f32_32x32x16_bf16 v[192:207], v[212:215], v[128:131], v[192:207]
	ds_read_b128 v[212:215], v246 offset:8192
	s_waitcnt lgkmcnt(7)
	v_mfma_f32_32x32x16_bf16 v[176:191], v[216:219], v[132:135], v[176:191]
	ds_read_b128 v[216:219], v247
	s_waitcnt lgkmcnt(7)
	v_mfma_f32_32x32x16_bf16 v[192:207], v[220:223], v[132:135], v[192:207]
	ds_read_b128 v[220:223], v247 offset:8192
	s_waitcnt lgkmcnt(7)
	v_mfma_f32_32x32x16_bf16 v[176:191], v[224:227], v[136:139], v[176:191]
	ds_read_b128 v[224:227], v248
	s_waitcnt lgkmcnt(7)
	v_mfma_f32_32x32x16_bf16 v[192:207], v[234:237], v[136:139], v[192:207]
	ds_read_b128 v[234:237], v248 offset:8192
	s_waitcnt lgkmcnt(7)
	v_mfma_f32_32x32x16_bf16 v[176:191], v[238:241], v[140:143], v[176:191]
	ds_read_b128 v[238:241], v249
	s_waitcnt lgkmcnt(7)
	v_mfma_f32_32x32x16_bf16 v[192:207], v[242:245], v[140:143], v[192:207]
	ds_read_b128 v[242:245], v249 offset:8192
	s_add_i32 s6, s65, -1
	s_cmp_gt_i32 s6, s44
	s_cbranch_scc1 .Lat_pmask0
	s_cmp_lt_i32 s65, 0xb0
	s_cbranch_scc0 .Lat_pnomask0
.Lat_pmask0:
	s_nop 13
	v_add_u32_e32 v152, 64, v147
	v_cmp_lt_u32_e32 vcc, v152, v163
	v_subrev_u32_e32 v0, 32, v152
	s_nop 0
	v_cndmask_b32_e32 v176, v160, v176, vcc
	v_cmp_lt_u32_e32 vcc, v0, v163
	v_subrev_u32_e32 v0, 1, v152
	s_nop 0
	v_cndmask_b32_e32 v192, v160, v192, vcc
	v_cmp_lt_u32_e32 vcc, v0, v163
	v_subrev_u32_e32 v0, 33, v152
	s_nop 0
	v_cndmask_b32_e32 v177, v160, v177, vcc
	v_cmp_lt_u32_e32 vcc, v0, v163
	v_subrev_u32_e32 v0, 2, v152
	s_nop 0
	v_cndmask_b32_e32 v193, v160, v193, vcc
	v_cmp_lt_u32_e32 vcc, v0, v163
	v_subrev_u32_e32 v0, 34, v152
	s_nop 0
	v_cndmask_b32_e32 v178, v160, v178, vcc
	v_cmp_lt_u32_e32 vcc, v0, v163
	v_subrev_u32_e32 v0, 3, v152
	s_nop 0
	v_cndmask_b32_e32 v194, v160, v194, vcc
	v_cmp_lt_u32_e32 vcc, v0, v163
	v_subrev_u32_e32 v0, 35, v152
	s_nop 0
	v_cndmask_b32_e32 v179, v160, v179, vcc
	v_cmp_lt_u32_e32 vcc, v0, v163
	v_subrev_u32_e32 v0, 8, v152
	s_nop 0
	v_cndmask_b32_e32 v195, v160, v195, vcc
	v_cmp_lt_u32_e32 vcc, v0, v163
	v_subrev_u32_e32 v0, 40, v152
	s_nop 0
	v_cndmask_b32_e32 v180, v160, v180, vcc
	v_cmp_lt_u32_e32 vcc, v0, v163
	v_subrev_u32_e32 v0, 9, v152
	s_nop 0
	v_cndmask_b32_e32 v196, v160, v196, vcc
	v_cmp_lt_u32_e32 vcc, v0, v163
	v_subrev_u32_e32 v0, 41, v152
	s_nop 0
	v_cndmask_b32_e32 v181, v160, v181, vcc
	v_cmp_lt_u32_e32 vcc, v0, v163
	v_subrev_u32_e32 v0, 10, v152
	s_nop 0
	v_cndmask_b32_e32 v197, v160, v197, vcc
	v_cmp_lt_u32_e32 vcc, v0, v163
	v_subrev_u32_e32 v0, 42, v152
	s_nop 0
	v_cndmask_b32_e32 v182, v160, v182, vcc
	v_cmp_lt_u32_e32 vcc, v0, v163
	v_subrev_u32_e32 v0, 11, v152
	s_nop 0
	v_cndmask_b32_e32 v198, v160, v198, vcc
	v_cmp_lt_u32_e32 vcc, v0, v163
	v_subrev_u32_e32 v0, 43, v152
	s_nop 0
	v_cndmask_b32_e32 v183, v160, v183, vcc
	v_cmp_lt_u32_e32 vcc, v0, v163
	v_subrev_u32_e32 v0, 16, v152
	s_nop 0
	v_cndmask_b32_e32 v199, v160, v199, vcc
	v_cmp_lt_u32_e32 vcc, v0, v163
	v_subrev_u32_e32 v0, 48, v152
	s_nop 0
	v_cndmask_b32_e32 v184, v160, v184, vcc
	v_cmp_lt_u32_e32 vcc, v0, v163
	v_subrev_u32_e32 v0, 17, v152
	s_nop 0
	v_cndmask_b32_e32 v200, v160, v200, vcc
	v_cmp_lt_u32_e32 vcc, v0, v163
	v_subrev_u32_e32 v0, 49, v152
	s_nop 0
	v_cndmask_b32_e32 v185, v160, v185, vcc
	v_cmp_lt_u32_e32 vcc, v0, v163
	v_subrev_u32_e32 v0, 18, v152
	s_nop 0
	v_cndmask_b32_e32 v201, v160, v201, vcc
	v_cmp_lt_u32_e32 vcc, v0, v163
	v_subrev_u32_e32 v0, 50, v152
	s_nop 0
	v_cndmask_b32_e32 v186, v160, v186, vcc
	v_cmp_lt_u32_e32 vcc, v0, v163
	v_subrev_u32_e32 v0, 19, v152
	s_nop 0
	v_cndmask_b32_e32 v202, v160, v202, vcc
	v_cmp_lt_u32_e32 vcc, v0, v163
	v_subrev_u32_e32 v0, 51, v152
	s_nop 0
	v_cndmask_b32_e32 v187, v160, v187, vcc
	v_cmp_lt_u32_e32 vcc, v0, v163
	v_subrev_u32_e32 v0, 24, v152
	s_nop 0
	v_cndmask_b32_e32 v203, v160, v203, vcc
	v_cmp_lt_u32_e32 vcc, v0, v163
	v_subrev_u32_e32 v0, 56, v152
	s_nop 0
	v_cndmask_b32_e32 v188, v160, v188, vcc
	v_cmp_lt_u32_e32 vcc, v0, v163
	v_subrev_u32_e32 v0, 25, v152
	s_nop 0
	v_cndmask_b32_e32 v204, v160, v204, vcc
	v_cmp_lt_u32_e32 vcc, v0, v163
	v_subrev_u32_e32 v0, 57, v152
	s_nop 0
	v_cndmask_b32_e32 v189, v160, v189, vcc
	v_cmp_lt_u32_e32 vcc, v0, v163
	v_subrev_u32_e32 v0, 26, v152
	s_nop 0
	v_cndmask_b32_e32 v205, v160, v205, vcc
	v_cmp_lt_u32_e32 vcc, v0, v163
	v_subrev_u32_e32 v0, 58, v152
	s_nop 0
	v_cndmask_b32_e32 v190, v160, v190, vcc
	v_cmp_lt_u32_e32 vcc, v0, v163
	v_subrev_u32_e32 v0, 27, v152
	s_nop 0
	v_cndmask_b32_e32 v206, v160, v206, vcc
	v_cmp_lt_u32_e32 vcc, v0, v163
	v_subrev_u32_e32 v0, 59, v152
	s_nop 0
	v_cndmask_b32_e32 v191, v160, v191, vcc
	v_cmp_lt_u32_e32 vcc, v0, v163
	s_nop 0
	s_nop 0
	v_cndmask_b32_e32 v207, v160, v207, vcc
.Lat_pnomask0:
	s_nop 13
	v_max3_f32 v0, v176, v177, v178
	v_max3_f32 v2, v184, v185, v186
	v_max3_f32 v3, v192, v193, v194
	v_max3_f32 v4, v200, v201, v202
	v_max3_f32 v0, v0, v179, v180
	v_max3_f32 v2, v2, v187, v188
	v_max3_f32 v3, v3, v195, v196
	v_max3_f32 v4, v4, v203, v204
	v_max3_f32 v0, v0, v181, v182
	v_max3_f32 v2, v2, v189, v190
	v_max3_f32 v3, v3, v197, v198
	v_max3_f32 v4, v4, v205, v206
	v_max_f32_e32 v0, v0, v183
	v_max_f32_e32 v2, v2, v191
	v_max_f32_e32 v3, v3, v199
	v_max_f32_e32 v4, v4, v207
	v_max3_f32 v0, v0, v2, v3
	v_max_f32_e32 v0, v0, v4
	v_mov_b32_e32 v2, v0
	s_nop 1
	v_permlane32_swap_b32_e32 v0, v2
	v_max_f32_e32 v2, v2, v2
	v_max_f32_e32 v0, v0, v0
	v_max_f32_e32 v0, v0, v2
	v_sub_f32_e32 v2, v0, v173
	v_mul_f32_e32 v2, 0x3db504f3, v2
	v_cmp_ge_f32_e32 vcc, s63, v2
	v_max_f32_e32 v2, v173, v173
	v_max_f32_e32 v2, v2, v0
	v_sub_f32_e32 v0, v173, v2
	v_mul_f32_e32 v0, 0x3e0293ee, v0
	v_exp_f32_e32 v0, v0
	s_cmp_eq_u64 vcc, exec
	s_cselect_b64 s[6:7], -1, 0
	v_cndmask_b32_e64 v0, v0, 1.0, s[6:7]
	v_cmp_gt_f32_e32 vcc, 1.0, v0
	v_mov_b32_e32 v233, v0
	v_cndmask_b32_e64 v173, v2, v173, s[6:7]
	s_cmp_lg_u64 vcc, 0
	s_cselect_b32 s99, 1, 0
	v_mul_f32_e32 v2, 0xbe0293ee, v173
	v_fmamk_f32 v176, v176, 0x3e0293ee, v2
	v_fmamk_f32 v177, v177, 0x3e0293ee, v2
	v_fmamk_f32 v178, v178, 0x3e0293ee, v2
	v_fmamk_f32 v179, v179, 0x3e0293ee, v2
	v_fmamk_f32 v180, v180, 0x3e0293ee, v2
	v_fmamk_f32 v181, v181, 0x3e0293ee, v2
	v_fmamk_f32 v182, v182, 0x3e0293ee, v2
	v_fmamk_f32 v183, v183, 0x3e0293ee, v2
	v_fmamk_f32 v184, v184, 0x3e0293ee, v2
	v_fmamk_f32 v185, v185, 0x3e0293ee, v2
	v_fmamk_f32 v186, v186, 0x3e0293ee, v2
	v_fmamk_f32 v187, v187, 0x3e0293ee, v2
	v_fmamk_f32 v188, v188, 0x3e0293ee, v2
	v_fmamk_f32 v189, v189, 0x3e0293ee, v2
	v_fmamk_f32 v190, v190, 0x3e0293ee, v2
	v_fmamk_f32 v191, v191, 0x3e0293ee, v2
	v_exp_f32_e32 v176, v176
	v_fmamk_f32 v192, v192, 0x3e0293ee, v2
	v_exp_f32_e32 v177, v177
	v_fmamk_f32 v193, v193, 0x3e0293ee, v2
	v_exp_f32_e32 v178, v178
	v_fmamk_f32 v194, v194, 0x3e0293ee, v2
	v_exp_f32_e32 v179, v179
	v_fmamk_f32 v195, v195, 0x3e0293ee, v2
	v_exp_f32_e32 v180, v180
	v_fmamk_f32 v196, v196, 0x3e0293ee, v2
	v_exp_f32_e32 v181, v181
	v_fmamk_f32 v197, v197, 0x3e0293ee, v2
	v_exp_f32_e32 v182, v182
	v_fmamk_f32 v198, v198, 0x3e0293ee, v2
	v_exp_f32_e32 v183, v183
	v_fmamk_f32 v199, v199, 0x3e0293ee, v2
	v_exp_f32_e32 v184, v184
	v_fmamk_f32 v200, v200, 0x3e0293ee, v2
	v_exp_f32_e32 v185, v185
	v_fmamk_f32 v201, v201, 0x3e0293ee, v2
	v_exp_f32_e32 v186, v186
	v_fmamk_f32 v202, v202, 0x3e0293ee, v2
	v_exp_f32_e32 v187, v187
	v_fmamk_f32 v203, v203, 0x3e0293ee, v2
	v_exp_f32_e32 v188, v188
	v_fmamk_f32 v204, v204, 0x3e0293ee, v2
	v_exp_f32_e32 v189, v189
	v_fmamk_f32 v205, v205, 0x3e0293ee, v2
	v_exp_f32_e32 v190, v190
	v_fmamk_f32 v206, v206, 0x3e0293ee, v2
	v_exp_f32_e32 v191, v191
	v_fmamk_f32 v207, v207, 0x3e0293ee, v2
	s_add_i32 s6, s45, 2
	s_and_b32 s6, s6, 3
	s_lshl_b32 s6, s6, 8
	s_add_i32 s6, s6, 0x10800
	v_add_u32_e32 v152, s6, v164
	ds_read_b128 v[96:99], v152
	ds_read_b128 v[100:103], v152 offset:32
	ds_read_b128 v[80:83], v152 offset:128
	ds_read_b128 v[84:87], v152 offset:160
	ds_read_b128 v[104:107], v152 offset:64
	ds_read_b128 v[108:111], v152 offset:96
	ds_read_b128 v[88:91], v152 offset:192
	ds_read_b128 v[92:95], v152 offset:224
	s_branch .Lat_turn_end0
.Lat_steady0:
	s_waitcnt lgkmcnt(0)
	v_add3_u32 v246, v166, v165, s42
	v_add3_u32 v247, v168, v165, s42
	v_add3_u32 v248, v169, v165, s42
	v_add3_u32 v249, v170, v165, s42
	v_add_u32_e32 v153, s66, v162
	v_mfma_f32_32x32x16_bf16 v[176:191], v[208:211], v[112:115], v[176:191]
	ds_read_b128 v[208:211], v246 offset:128
	v_exp_f32_e32 v80, v80
	v_exp_f32_e32 v81, v81
	v_add_f32_e32 v148, v96, v100
	v_add_f32_e32 v149, v97, v101
	v_mfma_f32_32x32x16_bf16 v[192:207], v[212:215], v[112:115], v[192:207]
	ds_read_b128 v[212:215], v246 offset:8320
	v_exp_f32_e32 v82, v82
	v_exp_f32_e32 v83, v83
	v_add_f32_e32 v150, v98, v102
	v_add_f32_e32 v151, v99, v103
	v_mfma_f32_32x32x16_bf16 v[176:191], v[216:219], v[116:119], v[176:191]
	ds_read_b128 v[216:219], v247 offset:128
	v_exp_f32_e32 v84, v84
	v_exp_f32_e32 v85, v85
	v_add_f32_e32 v148, v148, v104
	v_add_f32_e32 v149, v149, v105
	v_mfma_f32_32x32x16_bf16 v[192:207], v[220:223], v[116:119], v[192:207]
	ds_read_b128 v[220:223], v247 offset:8320
	v_exp_f32_e32 v86, v86
	v_exp_f32_e32 v87, v87
	v_add_f32_e32 v150, v150, v106
	v_add_f32_e32 v151, v151, v107
	v_mfma_f32_32x32x16_bf16 v[176:191], v[224:227], v[120:123], v[176:191]
	ds_read_b128 v[224:227], v248 offset:128
	v_exp_f32_e32 v88, v88
	v_exp_f32_e32 v89, v89
	v_add_f32_e32 v148, v148, v108
	v_add_f32_e32 v149, v149, v109
	v_mfma_f32_32x32x16_bf16 v[192:207], v[234:237], v[120:123], v[192:207]
	ds_read_b128 v[234:237], v248 offset:8320
	v_exp_f32_e32 v90, v90
	v_exp_f32_e32 v91, v91
	v_add_f32_e32 v150, v150, v110
	v_add_f32_e32 v151, v151, v111
	v_mfma_f32_32x32x16_bf16 v[176:191], v[238:241], v[124:127], v[176:191]
	ds_read_b128 v[238:241], v249 offset:128
	v_exp_f32_e32 v92, v92
	v_exp_f32_e32 v93, v93
	v_add_f32_e32 v148, v148, v80
	v_add_f32_e32 v149, v149, v81
	v_mfma_f32_32x32x16_bf16 v[192:207], v[242:245], v[124:127], v[192:207]
	ds_read_b128 v[242:245], v249 offset:8320
	v_exp_f32_e32 v94, v94
	v_exp_f32_e32 v95, v95
	v_add_f32_e32 v150, v150, v82
	v_add_f32_e32 v151, v151, v83
	s_waitcnt lgkmcnt(7)
	v_mfma_f32_32x32x16_bf16 v[176:191], v[208:211], v[128:131], v[176:191]
	ds_read_b64_tr_b16 v[208:209], v153 offset:0
	ds_read_b64_tr_b16 v[210:211], v153 offset:2048
	v_add_f32_e32 v148, v148, v84
	v_add_f32_e32 v149, v149, v85
	v_add_f32_e32 v150, v150, v86
	v_add_f32_e32 v151, v151, v87
	v_add_f32_e32 v148, v148, v88
	v_add_f32_e32 v149, v149, v89
	s_waitcnt lgkmcnt(8)
	v_mfma_f32_32x32x16_bf16 v[192:207], v[212:215], v[128:131], v[192:207]
	ds_read_b64_tr_b16 v[212:213], v153 offset:512
	ds_read_b64_tr_b16 v[214:215], v153 offset:2560
	v_add_f32_e32 v150, v150, v90
	v_add_f32_e32 v151, v151, v91
	v_add_f32_e32 v148, v148, v92
	v_add_f32_e32 v149, v149, v93
	v_add_f32_e32 v150, v150, v94
	v_add_f32_e32 v151, v151, v95
	s_waitcnt lgkmcnt(9)
	v_mfma_f32_32x32x16_bf16 v[176:191], v[216:219], v[132:135], v[176:191]
	ds_read_b64_tr_b16 v[216:217], v153 offset:1024
	ds_read_b64_tr_b16 v[218:219], v153 offset:3072
	v_add_f32_e32 v148, v148, v149
	v_add_f32_e32 v150, v150, v151
	v_add_f32_e32 v148, v148, v150
	v_mov_b32_e32 v152, v148
	v_cvt_pk_bf16_f32 v96, v96, v97
	v_cvt_pk_bf16_f32 v97, v98, v99
	s_waitcnt lgkmcnt(10)
	v_mfma_f32_32x32x16_bf16 v[192:207], v[220:223], v[132:135], v[192:207]
	ds_read_b64_tr_b16 v[220:221], v153 offset:1536
	ds_read_b64_tr_b16 v[222:223], v153 offset:3584
	v_permlane32_swap_b32_e32 v148, v152
	v_cvt_pk_bf16_f32 v98, v100, v101
	v_cvt_pk_bf16_f32 v99, v102, v103
	v_add_f32_e32 v148, v148, v152
	v_cvt_pk_bf16_f32 v100, v104, v105
	v_cvt_pk_bf16_f32 v101, v106, v107
	s_waitcnt lgkmcnt(11)
	v_mfma_f32_32x32x16_bf16 v[176:191], v[224:227], v[136:139], v[176:191]
	ds_read_b64_tr_b16 v[224:225], v153 offset:4096
	ds_read_b64_tr_b16 v[226:227], v153 offset:6144
	v_cvt_pk_bf16_f32 v102, v108, v109
	v_cvt_pk_bf16_f32 v103, v110, v111
	v_cvt_pk_bf16_f32 v104, v80, v81
	v_cvt_pk_bf16_f32 v105, v82, v83
	v_cvt_pk_bf16_f32 v106, v84, v85
	v_cvt_pk_bf16_f32 v107, v86, v87
	s_waitcnt lgkmcnt(12)
	v_mfma_f32_32x32x16_bf16 v[192:207], v[234:237], v[136:139], v[192:207]
	ds_read_b64_tr_b16 v[234:235], v153 offset:4608
	ds_read_b64_tr_b16 v[236:237], v153 offset:6656
	v_cvt_pk_bf16_f32 v108, v88, v89
	v_cvt_pk_bf16_f32 v109, v90, v91
	v_cvt_pk_bf16_f32 v110, v92, v93
	v_cvt_pk_bf16_f32 v111, v94, v95
	v_fma_f32 v174, v174, v233, v148
	s_nop 0
	s_waitcnt lgkmcnt(13)
	v_mfma_f32_32x32x16_bf16 v[176:191], v[238:241], v[140:143], v[176:191]
	ds_read_b64_tr_b16 v[238:239], v153 offset:5120
	ds_read_b64_tr_b16 v[240:241], v153 offset:7168
	v_permlane32_swap_b32_e32 v96, v98
	v_permlane32_swap_b32_e32 v97, v99
	v_permlane32_swap_b32_e32 v100, v102
	v_permlane32_swap_b32_e32 v101, v103
	v_permlane32_swap_b32_e32 v104, v106
	v_permlane32_swap_b32_e32 v105, v107
	s_waitcnt lgkmcnt(14)
	v_mfma_f32_32x32x16_bf16 v[192:207], v[242:245], v[140:143], v[192:207]
	ds_read_b64_tr_b16 v[242:243], v153 offset:5632
	ds_read_b64_tr_b16 v[244:245], v153 offset:7680
	v_permlane32_swap_b32_e32 v108, v110
	v_permlane32_swap_b32_e32 v109, v111
	s_add_i32 s6, s65, -1
	s_cmp_gt_i32 s6, s44
	s_cbranch_scc1 .Lat_mask0
	s_cmp_lt_i32 s65, 0xb0
	s_cbranch_scc0 .Lat_nomask0

.Lat_nomask0:
	s_cmp_eq_u32 s99, 0
	s_cbranch_scc1 .Lat_norescale0
	s_and_saveexec_b64 vcc, s[4:5]
	ds_write_b32 v167, v233 offset:128
	s_or_b64 exec, exec, vcc
	s_waitcnt lgkmcnt(0)
	ds_read_b128 v[2:5], v161 offset:224
	ds_read_b128 v[6:9], v161 offset:192
	ds_read_b128 v[10:13], v161 offset:160
	ds_read_b128 v[148:151], v161 offset:128
	s_waitcnt lgkmcnt(0)
	v_pk_mul_f32 v[78:79], v[78:79], v[4:5]
	v_pk_mul_f32 v[74:75], v[74:75], v[8:9]
	v_pk_mul_f32 v[70:71], v[70:71], v[12:13]
	v_pk_mul_f32 v[66:67], v[66:67], v[150:151]
	v_pk_mul_f32 v[76:77], v[76:77], v[2:3]
	v_pk_mul_f32 v[72:73], v[72:73], v[6:7]
	v_pk_mul_f32 v[68:69], v[68:69], v[10:11]
	v_pk_mul_f32 v[64:65], v[64:65], v[148:149]
	v_pk_mul_f32 v[62:63], v[62:63], v[4:5]
	v_pk_mul_f32 v[58:59], v[58:59], v[8:9]
	v_pk_mul_f32 v[54:55], v[54:55], v[12:13]
	v_pk_mul_f32 v[50:51], v[50:51], v[150:151]
	v_pk_mul_f32 v[60:61], v[60:61], v[2:3]
	v_pk_mul_f32 v[56:57], v[56:57], v[6:7]
	v_pk_mul_f32 v[52:53], v[52:53], v[10:11]
	v_pk_mul_f32 v[48:49], v[48:49], v[148:149]
	v_pk_mul_f32 v[46:47], v[46:47], v[4:5]
	v_pk_mul_f32 v[42:43], v[42:43], v[8:9]
	v_pk_mul_f32 v[38:39], v[38:39], v[12:13]
	v_pk_mul_f32 v[34:35], v[34:35], v[150:151]
	v_pk_mul_f32 v[44:45], v[44:45], v[2:3]
	v_pk_mul_f32 v[40:41], v[40:41], v[6:7]
	v_pk_mul_f32 v[36:37], v[36:37], v[10:11]
	v_pk_mul_f32 v[32:33], v[32:33], v[148:149]
	v_pk_mul_f32 v[30:31], v[30:31], v[4:5]
	v_pk_mul_f32 v[26:27], v[26:27], v[8:9]
	v_pk_mul_f32 v[22:23], v[22:23], v[12:13]
	v_pk_mul_f32 v[18:19], v[18:19], v[150:151]
	v_pk_mul_f32 v[28:29], v[28:29], v[2:3]
	v_pk_mul_f32 v[24:25], v[24:25], v[6:7]
	v_pk_mul_f32 v[20:21], v[20:21], v[10:11]
	v_pk_mul_f32 v[16:17], v[16:17], v[148:149]
.Lat_norescale0:
	v_add3_u32 v246, v166, v165, s43
	v_add3_u32 v247, v168, v165, s43
	v_add3_u32 v248, v169, v165, s43
	v_add3_u32 v249, v170, v165, s43
	s_add_i32 s6, s45, 2
	s_and_b32 s6, s6, 3
	s_lshl_b32 s6, s6, 8
	s_add_i32 s6, s6, 0x10800
	v_add_u32_e32 v152, s6, v164
	s_add_i32 s6, s45, 1
	s_cmp_ge_u32 s6, s46
	s_cbranch_scc1 .Lat_p2last0
	s_waitcnt lgkmcnt(14)
	v_mfma_f32_32x32x16_bf16 v[64:79], v[96:99], v[208:211], v[64:79]
	ds_read_b64_tr_b16 v[208:209], v153 offset:8192
	ds_read_b64_tr_b16 v[210:211], v153 offset:10240
	ds_read_b128 v[80:83], v152 offset:128
	s_waitcnt lgkmcnt(15)
	v_mfma_f32_32x32x16_bf16 v[48:63], v[96:99], v[212:215], v[48:63]
	ds_read_b64_tr_b16 v[212:213], v153 offset:8704
	ds_read_b64_tr_b16 v[214:215], v153 offset:10752
	ds_read_b128 v[84:87], v152 offset:160
	v_max3_f32 v0, v176, v177, v178
	v_max3_f32 v2, v184, v185, v186
	v_max3_f32 v3, v192, v193, v194
	v_max3_f32 v4, v200, v201, v202
	v_max3_f32 v0, v0, v179, v180
	v_max3_f32 v2, v2, v187, v188
	s_waitcnt lgkmcnt(15)
	v_mfma_f32_32x32x16_bf16 v[32:47], v[96:99], v[216:219], v[32:47]
	ds_read_b64_tr_b16 v[216:217], v153 offset:9216
	ds_read_b64_tr_b16 v[218:219], v153 offset:11264
	ds_read_b128 v[88:91], v152 offset:192
	v_max3_f32 v3, v3, v195, v196
	v_max3_f32 v4, v4, v203, v204
	v_max3_f32 v0, v0, v181, v182
	v_max3_f32 v2, v2, v189, v190
	v_max3_f32 v3, v3, v197, v198
	v_max3_f32 v4, v4, v205, v206
	s_waitcnt lgkmcnt(15)
	v_mfma_f32_32x32x16_bf16 v[16:31], v[96:99], v[220:223], v[16:31]
	ds_read_b64_tr_b16 v[220:221], v153 offset:9728
	ds_read_b64_tr_b16 v[222:223], v153 offset:11776
	ds_read_b128 v[92:95], v152 offset:224
	ds_read_b128 v[96:99], v152
	v_max_f32_e32 v0, v0, v183
	v_max_f32_e32 v2, v2, v191
	v_max_f32_e32 v3, v3, v199
	v_max_f32_e32 v4, v4, v207
	v_max3_f32 v0, v0, v2, v3
	v_max_f32_e32 v0, v0, v4
	s_waitcnt lgkmcnt(15)
	v_mfma_f32_32x32x16_bf16 v[64:79], v[100:103], v[224:227], v[64:79]
	ds_read_b64_tr_b16 v[224:225], v153 offset:12288
	ds_read_b64_tr_b16 v[226:227], v153 offset:14336
	v_mov_b32_e32 v2, v0
	s_nop 1
	v_permlane32_swap_b32_e32 v0, v2
	v_max_f32_e32 v2, v2, v2
	v_max_f32_e32 v0, v0, v0
	s_waitcnt lgkmcnt(15)
	v_mfma_f32_32x32x16_bf16 v[48:63], v[100:103], v[234:237], v[48:63]
	ds_read_b64_tr_b16 v[234:235], v153 offset:12800
	ds_read_b64_tr_b16 v[236:237], v153 offset:14848
	v_max_f32_e32 v0, v0, v2
	v_sub_f32_e32 v2, v0, v173
	v_mul_f32_e32 v2, 0x3db504f3, v2
	v_cmp_ge_f32_e32 vcc, s63, v2
	v_max_f32_e32 v2, v173, v173
	v_max_f32_e32 v2, v2, v0
	s_waitcnt lgkmcnt(15)
	v_mfma_f32_32x32x16_bf16 v[32:47], v[100:103], v[238:241], v[32:47]
	ds_read_b64_tr_b16 v[238:239], v153 offset:13312
	ds_read_b64_tr_b16 v[240:241], v153 offset:15360
	v_sub_f32_e32 v0, v173, v2
	v_mul_f32_e32 v0, 0x3e0293ee, v0
	v_exp_f32_e32 v0, v0
	s_cmp_eq_u64 vcc, exec
	s_cselect_b64 s[6:7], -1, 0
	v_cndmask_b32_e64 v0, v0, 1.0, s[6:7]
	s_waitcnt lgkmcnt(15)
	v_mfma_f32_32x32x16_bf16 v[16:31], v[100:103], v[242:245], v[16:31]
	ds_read_b64_tr_b16 v[242:243], v153 offset:13824
	ds_read_b64_tr_b16 v[244:245], v153 offset:15872
	ds_read_b128 v[100:103], v152 offset:32
	v_cmp_gt_f32_e32 vcc, 1.0, v0
	v_mov_b32_e32 v233, v0
	v_cndmask_b32_e64 v173, v2, v173, s[6:7]
	s_cmp_lg_u64 vcc, 0
	s_cselect_b32 s99, 1, 0
	v_mul_f32_e32 v2, 0xbe0293ee, v173
	v_fmamk_f32 v176, v176, 0x3e0293ee, v2
	s_waitcnt lgkmcnt(15)
	v_mfma_f32_32x32x16_bf16 v[64:79], v[104:107], v[208:211], v[64:79]
	ds_read_b128 v[208:211], v246
	v_fmamk_f32 v177, v177, 0x3e0293ee, v2
	v_fmamk_f32 v178, v178, 0x3e0293ee, v2
	v_fmamk_f32 v179, v179, 0x3e0293ee, v2
	v_fmamk_f32 v180, v180, 0x3e0293ee, v2
	v_fmamk_f32 v181, v181, 0x3e0293ee, v2
	v_fmamk_f32 v182, v182, 0x3e0293ee, v2
	s_waitcnt lgkmcnt(15)
	v_mfma_f32_32x32x16_bf16 v[48:63], v[104:107], v[212:215], v[48:63]
	ds_read_b128 v[212:215], v246 offset:8192
	v_fmamk_f32 v183, v183, 0x3e0293ee, v2
	v_fmamk_f32 v184, v184, 0x3e0293ee, v2
	v_fmamk_f32 v185, v185, 0x3e0293ee, v2
	v_fmamk_f32 v186, v186, 0x3e0293ee, v2
	v_fmamk_f32 v187, v187, 0x3e0293ee, v2
	v_fmamk_f32 v188, v188, 0x3e0293ee, v2
	s_waitcnt lgkmcnt(15)
	v_mfma_f32_32x32x16_bf16 v[32:47], v[104:107], v[216:219], v[32:47]
	ds_read_b128 v[216:219], v247
	v_fmamk_f32 v189, v189, 0x3e0293ee, v2
	v_fmamk_f32 v190, v190, 0x3e0293ee, v2
	v_fmamk_f32 v191, v191, 0x3e0293ee, v2
	v_exp_f32_e32 v176, v176
	v_fmamk_f32 v192, v192, 0x3e0293ee, v2
	s_waitcnt lgkmcnt(14)
	v_mfma_f32_32x32x16_bf16 v[16:31], v[104:107], v[220:223], v[16:31]
	ds_read_b128 v[220:223], v247 offset:8192
	ds_read_b128 v[104:107], v152 offset:64
	v_exp_f32_e32 v177, v177
	v_fmamk_f32 v193, v193, 0x3e0293ee, v2
	v_exp_f32_e32 v178, v178
	v_fmamk_f32 v194, v194, 0x3e0293ee, v2
	s_waitcnt lgkmcnt(12)
	v_mfma_f32_32x32x16_bf16 v[64:79], v[108:111], v[224:227], v[64:79]
	ds_read_b128 v[224:227], v248
	v_exp_f32_e32 v179, v179
	v_fmamk_f32 v195, v195, 0x3e0293ee, v2
	v_exp_f32_e32 v180, v180
	v_fmamk_f32 v196, v196, 0x3e0293ee, v2
	s_waitcnt lgkmcnt(11)
	v_mfma_f32_32x32x16_bf16 v[48:63], v[108:111], v[234:237], v[48:63]
	ds_read_b128 v[234:237], v248 offset:8192
	v_exp_f32_e32 v181, v181
	v_fmamk_f32 v197, v197, 0x3e0293ee, v2
	v_exp_f32_e32 v182, v182
	v_fmamk_f32 v198, v198, 0x3e0293ee, v2
	s_waitcnt lgkmcnt(10)
	v_mfma_f32_32x32x16_bf16 v[32:47], v[108:111], v[238:241], v[32:47]
	ds_read_b128 v[238:241], v249
	v_exp_f32_e32 v183, v183
	v_fmamk_f32 v199, v199, 0x3e0293ee, v2
	v_exp_f32_e32 v184, v184
	v_fmamk_f32 v200, v200, 0x3e0293ee, v2
	s_waitcnt lgkmcnt(9)
	v_mfma_f32_32x32x16_bf16 v[16:31], v[108:111], v[242:245], v[16:31]
	ds_read_b128 v[242:245], v249 offset:8192
	ds_read_b128 v[108:111], v152 offset:96
	v_exp_f32_e32 v185, v185
	v_fmamk_f32 v201, v201, 0x3e0293ee, v2
	v_exp_f32_e32 v186, v186
	v_fmamk_f32 v202, v202, 0x3e0293ee, v2
	v_exp_f32_e32 v187, v187
	v_fmamk_f32 v203, v203, 0x3e0293ee, v2
	v_exp_f32_e32 v188, v188
	v_fmamk_f32 v204, v204, 0x3e0293ee, v2
	v_exp_f32_e32 v189, v189
	v_fmamk_f32 v205, v205, 0x3e0293ee, v2
	v_exp_f32_e32 v190, v190
	v_fmamk_f32 v206, v206, 0x3e0293ee, v2
	v_exp_f32_e32 v191, v191
	v_fmamk_f32 v207, v207, 0x3e0293ee, v2
	s_branch .Lat_turn_end0
.Lat_p2last0:
	s_waitcnt lgkmcnt(14)
	v_mfma_f32_32x32x16_bf16 v[64:79], v[96:99], v[208:211], v[64:79]
	ds_read_b64_tr_b16 v[208:209], v153 offset:8192
	ds_read_b64_tr_b16 v[210:211], v153 offset:10240
	ds_read_b128 v[80:83], v152 offset:128
	s_waitcnt lgkmcnt(15)
	v_mfma_f32_32x32x16_bf16 v[48:63], v[96:99], v[212:215], v[48:63]
	ds_read_b64_tr_b16 v[212:213], v153 offset:8704
	ds_read_b64_tr_b16 v[214:215], v153 offset:10752
	ds_read_b128 v[84:87], v152 offset:160
	s_waitcnt lgkmcnt(15)
	v_mfma_f32_32x32x16_bf16 v[32:47], v[96:99], v[216:219], v[32:47]
	ds_read_b64_tr_b16 v[216:217], v153 offset:9216
	ds_read_b64_tr_b16 v[218:219], v153 offset:11264
	ds_read_b128 v[88:91], v152 offset:192
	s_waitcnt lgkmcnt(15)
	v_mfma_f32_32x32x16_bf16 v[16:31], v[96:99], v[220:223], v[16:31]
	ds_read_b64_tr_b16 v[220:221], v153 offset:9728
	ds_read_b64_tr_b16 v[222:223], v153 offset:11776
	ds_read_b128 v[92:95], v152 offset:224
	ds_read_b128 v[96:99], v152
	s_waitcnt lgkmcnt(15)
	v_mfma_f32_32x32x16_bf16 v[64:79], v[100:103], v[224:227], v[64:79]
	ds_read_b64_tr_b16 v[224:225], v153 offset:12288
	ds_read_b64_tr_b16 v[226:227], v153 offset:14336
	s_waitcnt lgkmcnt(15)
	v_mfma_f32_32x32x16_bf16 v[48:63], v[100:103], v[234:237], v[48:63]
	ds_read_b64_tr_b16 v[234:235], v153 offset:12800
	ds_read_b64_tr_b16 v[236:237], v153 offset:14848
	s_waitcnt lgkmcnt(15)
	v_mfma_f32_32x32x16_bf16 v[32:47], v[100:103], v[238:241], v[32:47]
	ds_read_b64_tr_b16 v[238:239], v153 offset:13312
	ds_read_b64_tr_b16 v[240:241], v153 offset:15360
	s_waitcnt lgkmcnt(15)
	v_mfma_f32_32x32x16_bf16 v[16:31], v[100:103], v[242:245], v[16:31]
	ds_read_b64_tr_b16 v[242:243], v153 offset:13824
	ds_read_b64_tr_b16 v[244:245], v153 offset:15872
	ds_read_b128 v[100:103], v152 offset:32
	s_waitcnt lgkmcnt(15)
	v_mfma_f32_32x32x16_bf16 v[64:79], v[104:107], v[208:211], v[64:79]
	ds_read_b128 v[208:211], v246
	s_waitcnt lgkmcnt(15)
	v_mfma_f32_32x32x16_bf16 v[48:63], v[104:107], v[212:215], v[48:63]
	ds_read_b128 v[212:215], v246 offset:8192
	s_waitcnt lgkmcnt(15)
	v_mfma_f32_32x32x16_bf16 v[32:47], v[104:107], v[216:219], v[32:47]
	ds_read_b128 v[216:219], v247
	s_waitcnt lgkmcnt(14)
	v_mfma_f32_32x32x16_bf16 v[16:31], v[104:107], v[220:223], v[16:31]
	ds_read_b128 v[220:223], v247 offset:8192
	ds_read_b128 v[104:107], v152 offset:64
	s_waitcnt lgkmcnt(12)
	v_mfma_f32_32x32x16_bf16 v[64:79], v[108:111], v[224:227], v[64:79]
	ds_read_b128 v[224:227], v248
	s_waitcnt lgkmcnt(11)
	v_mfma_f32_32x32x16_bf16 v[48:63], v[108:111], v[234:237], v[48:63]
	ds_read_b128 v[234:237], v248 offset:8192
	s_waitcnt lgkmcnt(10)
	v_mfma_f32_32x32x16_bf16 v[32:47], v[108:111], v[238:241], v[32:47]
	ds_read_b128 v[238:241], v249
	s_waitcnt lgkmcnt(9)
	v_mfma_f32_32x32x16_bf16 v[16:31], v[108:111], v[242:245], v[16:31]
	ds_read_b128 v[242:245], v249 offset:8192
	ds_read_b128 v[108:111], v152 offset:96
.Lat_turn_end0:
	s_add_i32 s45, s45, 1
	s_addk_i32 s65, 0xffc0
	s_cmp_eq_u32 s66, 0
	s_cselect_b32 s7, 0x4000, 0
	s_cmp_eq_u32 s66, 0x4000
	s_cselect_b32 s66, 0xc000, s7
	v_add_u32_e32 v147, 64, v147
	s_sub_u32 s38, s38, 0x40000
	s_subb_u32 s39, s39, 0
	s_sub_u32 s100, s100, 0x40000
	s_subb_u32 s101, s101, 0
	s_sub_u32 s40, s40, 0x100
	s_subb_u32 s41, s41, 0
	s_mov_b32 s7, s33
	s_mov_b32 s33, s42
	s_mov_b32 s42, s43
	s_mov_b32 s43, s47
	s_mov_b32 s47, s7
	s_cmp_ge_u32 s68, 0x2000
	s_cbranch_scc0 .Lat_next0
	s_add_i32 s6, s45, 3
	s_cmp_lt_u32 s6, s46
	s_cbranch_scc1 .Lat_w90
	s_add_i32 s6, s45, 1
	s_cmp_lt_u32 s6, s46
	s_cbranch_scc1 .Lat_w40
	s_waitcnt vmcnt(0)
	s_branch .Lat_wd0
.Lat_w90:
	s_waitcnt vmcnt(9)
	s_branch .Lat_wd0
.Lat_w40:
	s_waitcnt vmcnt(4)
.Lat_wd0:
	s_cmp_lg_u32 s68, 0x2000
	s_cbranch_scc1 .Lat_next0
	s_add_i32 s6, s45, 2
	s_cmp_ge_u32 s6, s46
	s_cbranch_scc1 .Lat_next0
	s_cmp_lt_u32 s45, 1
	s_cbranch_scc1 .Lat_next0
	s_and_b32 s7, s6, 3
	s_lshl_b32 s7, s7, 8
	v_add_u32_e32 v0, s7, v171
	ds_write_b32 v0, v156
.Lat_next0:
	s_cmp_lt_u32 s45, s46
	s_cbranch_scc0 .Lat_done
.Lat_tile1:
	s_waitcnt lgkmcnt(0)
	s_barrier
	s_cmp_ge_u32 s68, 0x2000
	s_cbranch_scc0 .Lat_go1
	s_add_i32 s6, s45, 2
	s_cmp_ge_u32 s6, s46
	s_cbranch_scc1 .Lat_go1
	s_cmp_eq_u32 s66, 0
	s_cselect_b32 s6, 0xc000, 0
	s_cmp_eq_u32 s66, 0xc000
	s_cselect_b32 s6, 0x4000, s6
	s_add_i32 s6, s6, s98
	s_mov_b32 s7, s6
	s_mov_b32 m0, s7
	s_add_i32 s7, s7, 0x400
	global_load_lds_dwordx4 v228, s[38:39]
	s_mov_b32 m0, s7
	s_add_i32 s7, s7, 0x400
	global_load_lds_dwordx4 v229, s[38:39]
	s_mov_b32 m0, s7
	s_add_i32 s7, s7, 0x400
	global_load_lds_dwordx4 v230, s[38:39]
	s_mov_b32 m0, s7
	s_nop 0
	global_load_lds_dwordx4 v231, s[38:39]
	s_add_i32 s6, s45, 4
	s_cmp_ge_u32 s6, s46
	s_cbranch_scc1 .Lat_go1
	s_add_i32 s6, s33, s98
	s_mov_b32 s7, s6
	s_mov_b32 m0, s7
	s_add_i32 s7, s7, 0x400
	global_load_lds_dwordx4 v14, s[100:101]
	s_mov_b32 m0, s7
	s_add_i32 s7, s7, 0x400
	global_load_lds_dwordx4 v15, s[100:101]
	s_mov_b32 m0, s7
	s_add_i32 s7, s7, 0x400
	global_load_lds_dwordx4 v175, s[100:101]
	s_mov_b32 m0, s7
	s_nop 0
	global_load_lds_dwordx4 v155, s[100:101]
	global_load_dword v156, v232, s[40:41]
.Lat_go1:
	s_cmp_gt_i32 s65, s64
	s_cbranch_scc0 .Lat_steady1
	s_add_i32 s6, s65, 0xffffffc0
	s_cmp_gt_i32 s6, s64
	s_cbranch_scc1 .Lat_turn_end1
	s_add_i32 s6, s45, 1
	s_cmp_ge_u32 s6, s46
	s_cbranch_scc1 .Lat_turn_end1
	v_add3_u32 v246, v166, v165, s42
	v_add3_u32 v247, v168, v165, s42
	v_add3_u32 v248, v169, v165, s42
	v_add3_u32 v249, v170, v165, s42
	ds_read_b128 v[208:211], v246
	ds_read_b128 v[212:215], v246 offset:8192
	ds_read_b128 v[216:219], v247
	ds_read_b128 v[220:223], v247 offset:8192
	ds_read_b128 v[224:227], v248
	ds_read_b128 v[234:237], v248 offset:8192
	ds_read_b128 v[238:241], v249
	ds_read_b128 v[242:245], v249 offset:8192
	s_add_i32 s6, s45, 1
	s_and_b32 s6, s6, 3
	s_lshl_b32 s6, s6, 8
	s_add_i32 s6, s6, 0x10800
	v_add_u32_e32 v152, s6, v164
	ds_read_b128 v[96:99], v152
	ds_read_b128 v[100:103], v152 offset:32
	ds_read_b128 v[80:83], v152 offset:128
	ds_read_b128 v[84:87], v152 offset:160
	ds_read_b128 v[104:107], v152 offset:64
	ds_read_b128 v[108:111], v152 offset:96
	ds_read_b128 v[88:91], v152 offset:192
	ds_read_b128 v[92:95], v152 offset:224
	s_waitcnt lgkmcnt(0)
	v_mfma_f32_32x32x16_bf16 v[96:111], v[208:211], v[112:115], v[96:111]
	ds_read_b128 v[208:211], v246 offset:128
	v_mfma_f32_32x32x16_bf16 v[80:95], v[212:215], v[112:115], v[80:95]
	ds_read_b128 v[212:215], v246 offset:8320
	v_mfma_f32_32x32x16_bf16 v[96:111], v[216:219], v[116:119], v[96:111]
	ds_read_b128 v[216:219], v247 offset:128
	v_mfma_f32_32x32x16_bf16 v[80:95], v[220:223], v[116:119], v[80:95]
	ds_read_b128 v[220:223], v247 offset:8320
	v_mfma_f32_32x32x16_bf16 v[96:111], v[224:227], v[120:123], v[96:111]
	ds_read_b128 v[224:227], v248 offset:128
	v_mfma_f32_32x32x16_bf16 v[80:95], v[234:237], v[120:123], v[80:95]
	ds_read_b128 v[234:237], v248 offset:8320
	v_mfma_f32_32x32x16_bf16 v[96:111], v[238:241], v[124:127], v[96:111]
	ds_read_b128 v[238:241], v249 offset:128
	v_mfma_f32_32x32x16_bf16 v[80:95], v[242:245], v[124:127], v[80:95]
	ds_read_b128 v[242:245], v249 offset:8320
	s_waitcnt lgkmcnt(7)
	v_mfma_f32_32x32x16_bf16 v[96:111], v[208:211], v[128:131], v[96:111]
	v_add3_u32 v246, v166, v165, s43
	v_add3_u32 v247, v168, v165, s43
	v_add3_u32 v248, v169, v165, s43
	v_add3_u32 v249, v170, v165, s43
	ds_read_b128 v[208:211], v246
	s_waitcnt lgkmcnt(7)
	v_mfma_f32_32x32x16_bf16 v[80:95], v[212:215], v[128:131], v[80:95]
	ds_read_b128 v[212:215], v246 offset:8192
	s_waitcnt lgkmcnt(7)
	v_mfma_f32_32x32x16_bf16 v[96:111], v[216:219], v[132:135], v[96:111]
	ds_read_b128 v[216:219], v247
	s_waitcnt lgkmcnt(7)
	v_mfma_f32_32x32x16_bf16 v[80:95], v[220:223], v[132:135], v[80:95]
	ds_read_b128 v[220:223], v247 offset:8192
	s_waitcnt lgkmcnt(7)
	v_mfma_f32_32x32x16_bf16 v[96:111], v[224:227], v[136:139], v[96:111]
	ds_read_b128 v[224:227], v248
	s_waitcnt lgkmcnt(7)
	v_mfma_f32_32x32x16_bf16 v[80:95], v[234:237], v[136:139], v[80:95]
	ds_read_b128 v[234:237], v248 offset:8192
	s_waitcnt lgkmcnt(7)
	v_mfma_f32_32x32x16_bf16 v[96:111], v[238:241], v[140:143], v[96:111]
	ds_read_b128 v[238:241], v249
	s_waitcnt lgkmcnt(7)
	v_mfma_f32_32x32x16_bf16 v[80:95], v[242:245], v[140:143], v[80:95]
	ds_read_b128 v[242:245], v249 offset:8192
	s_add_i32 s6, s65, -1
	s_cmp_gt_i32 s6, s44
	s_cbranch_scc1 .Lat_pmask1
	s_cmp_lt_i32 s65, 0xb0
	s_cbranch_scc0 .Lat_pnomask1
.Lat_pmask1:
	s_nop 13
	v_add_u32_e32 v152, 64, v147
	v_cmp_lt_u32_e32 vcc, v152, v163
	v_subrev_u32_e32 v0, 32, v152
	s_nop 0
	v_cndmask_b32_e32 v96, v160, v96, vcc
	v_cmp_lt_u32_e32 vcc, v0, v163
	v_subrev_u32_e32 v0, 1, v152
	s_nop 0
	v_cndmask_b32_e32 v80, v160, v80, vcc
	v_cmp_lt_u32_e32 vcc, v0, v163
	v_subrev_u32_e32 v0, 33, v152
	s_nop 0
	v_cndmask_b32_e32 v97, v160, v97, vcc
	v_cmp_lt_u32_e32 vcc, v0, v163
	v_subrev_u32_e32 v0, 2, v152
	s_nop 0
	v_cndmask_b32_e32 v81, v160, v81, vcc
	v_cmp_lt_u32_e32 vcc, v0, v163
	v_subrev_u32_e32 v0, 34, v152
	s_nop 0
	v_cndmask_b32_e32 v98, v160, v98, vcc
	v_cmp_lt_u32_e32 vcc, v0, v163
	v_subrev_u32_e32 v0, 3, v152
	s_nop 0
	v_cndmask_b32_e32 v82, v160, v82, vcc
	v_cmp_lt_u32_e32 vcc, v0, v163
	v_subrev_u32_e32 v0, 35, v152
	s_nop 0
	v_cndmask_b32_e32 v99, v160, v99, vcc
	v_cmp_lt_u32_e32 vcc, v0, v163
	v_subrev_u32_e32 v0, 8, v152
	s_nop 0
	v_cndmask_b32_e32 v83, v160, v83, vcc
	v_cmp_lt_u32_e32 vcc, v0, v163
	v_subrev_u32_e32 v0, 40, v152
	s_nop 0
	v_cndmask_b32_e32 v100, v160, v100, vcc
	v_cmp_lt_u32_e32 vcc, v0, v163
	v_subrev_u32_e32 v0, 9, v152
	s_nop 0
	v_cndmask_b32_e32 v84, v160, v84, vcc
	v_cmp_lt_u32_e32 vcc, v0, v163
	v_subrev_u32_e32 v0, 41, v152
	s_nop 0
	v_cndmask_b32_e32 v101, v160, v101, vcc
	v_cmp_lt_u32_e32 vcc, v0, v163
	v_subrev_u32_e32 v0, 10, v152
	s_nop 0
	v_cndmask_b32_e32 v85, v160, v85, vcc
	v_cmp_lt_u32_e32 vcc, v0, v163
	v_subrev_u32_e32 v0, 42, v152
	s_nop 0
	v_cndmask_b32_e32 v102, v160, v102, vcc
	v_cmp_lt_u32_e32 vcc, v0, v163
	v_subrev_u32_e32 v0, 11, v152
	s_nop 0
	v_cndmask_b32_e32 v86, v160, v86, vcc
	v_cmp_lt_u32_e32 vcc, v0, v163
	v_subrev_u32_e32 v0, 43, v152
	s_nop 0
	v_cndmask_b32_e32 v103, v160, v103, vcc
	v_cmp_lt_u32_e32 vcc, v0, v163
	v_subrev_u32_e32 v0, 16, v152
	s_nop 0
	v_cndmask_b32_e32 v87, v160, v87, vcc
	v_cmp_lt_u32_e32 vcc, v0, v163
	v_subrev_u32_e32 v0, 48, v152
	s_nop 0
	v_cndmask_b32_e32 v104, v160, v104, vcc
	v_cmp_lt_u32_e32 vcc, v0, v163
	v_subrev_u32_e32 v0, 17, v152
	s_nop 0
	v_cndmask_b32_e32 v88, v160, v88, vcc
	v_cmp_lt_u32_e32 vcc, v0, v163
	v_subrev_u32_e32 v0, 49, v152
	s_nop 0
	v_cndmask_b32_e32 v105, v160, v105, vcc
	v_cmp_lt_u32_e32 vcc, v0, v163
	v_subrev_u32_e32 v0, 18, v152
	s_nop 0
	v_cndmask_b32_e32 v89, v160, v89, vcc
	v_cmp_lt_u32_e32 vcc, v0, v163
	v_subrev_u32_e32 v0, 50, v152
	s_nop 0
	v_cndmask_b32_e32 v106, v160, v106, vcc
	v_cmp_lt_u32_e32 vcc, v0, v163
	v_subrev_u32_e32 v0, 19, v152
	s_nop 0
	v_cndmask_b32_e32 v90, v160, v90, vcc
	v_cmp_lt_u32_e32 vcc, v0, v163
	v_subrev_u32_e32 v0, 51, v152
	s_nop 0
	v_cndmask_b32_e32 v107, v160, v107, vcc
	v_cmp_lt_u32_e32 vcc, v0, v163
	v_subrev_u32_e32 v0, 24, v152
	s_nop 0
	v_cndmask_b32_e32 v91, v160, v91, vcc
	v_cmp_lt_u32_e32 vcc, v0, v163
	v_subrev_u32_e32 v0, 56, v152
	s_nop 0
	v_cndmask_b32_e32 v108, v160, v108, vcc
	v_cmp_lt_u32_e32 vcc, v0, v163
	v_subrev_u32_e32 v0, 25, v152
	s_nop 0
	v_cndmask_b32_e32 v92, v160, v92, vcc
	v_cmp_lt_u32_e32 vcc, v0, v163
	v_subrev_u32_e32 v0, 57, v152
	s_nop 0
	v_cndmask_b32_e32 v109, v160, v109, vcc
	v_cmp_lt_u32_e32 vcc, v0, v163
	v_subrev_u32_e32 v0, 26, v152
	s_nop 0
	v_cndmask_b32_e32 v93, v160, v93, vcc
	v_cmp_lt_u32_e32 vcc, v0, v163
	v_subrev_u32_e32 v0, 58, v152
	s_nop 0
	v_cndmask_b32_e32 v110, v160, v110, vcc
	v_cmp_lt_u32_e32 vcc, v0, v163
	v_subrev_u32_e32 v0, 27, v152
	s_nop 0
	v_cndmask_b32_e32 v94, v160, v94, vcc
	v_cmp_lt_u32_e32 vcc, v0, v163
	v_subrev_u32_e32 v0, 59, v152
	s_nop 0
	v_cndmask_b32_e32 v111, v160, v111, vcc
	v_cmp_lt_u32_e32 vcc, v0, v163
	s_nop 0
	s_nop 0
	v_cndmask_b32_e32 v95, v160, v95, vcc
.Lat_pnomask1:
	s_nop 13
	v_max3_f32 v0, v96, v97, v98
	v_max3_f32 v2, v104, v105, v106
	v_max3_f32 v3, v80, v81, v82
	v_max3_f32 v4, v88, v89, v90
	v_max3_f32 v0, v0, v99, v100
	v_max3_f32 v2, v2, v107, v108
	v_max3_f32 v3, v3, v83, v84
	v_max3_f32 v4, v4, v91, v92
	v_max3_f32 v0, v0, v101, v102
	v_max3_f32 v2, v2, v109, v110
	v_max3_f32 v3, v3, v85, v86
	v_max3_f32 v4, v4, v93, v94
	v_max_f32_e32 v0, v0, v103
	v_max_f32_e32 v2, v2, v111
	v_max_f32_e32 v3, v3, v87
	v_max_f32_e32 v4, v4, v95
	v_max3_f32 v0, v0, v2, v3
	v_max_f32_e32 v0, v0, v4
	v_mov_b32_e32 v2, v0
	s_nop 1
	v_permlane32_swap_b32_e32 v0, v2
	v_max_f32_e32 v2, v2, v2
	v_max_f32_e32 v0, v0, v0
	v_max_f32_e32 v0, v0, v2
	v_sub_f32_e32 v2, v0, v173
	v_mul_f32_e32 v2, 0x3db504f3, v2
	v_cmp_ge_f32_e32 vcc, s63, v2
	v_max_f32_e32 v2, v173, v173
	v_max_f32_e32 v2, v2, v0
	v_sub_f32_e32 v0, v173, v2
	v_mul_f32_e32 v0, 0x3e0293ee, v0
	v_exp_f32_e32 v0, v0
	s_cmp_eq_u64 vcc, exec
	s_cselect_b64 s[6:7], -1, 0
	v_cndmask_b32_e64 v0, v0, 1.0, s[6:7]
	v_cmp_gt_f32_e32 vcc, 1.0, v0
	v_mov_b32_e32 v233, v0
	v_cndmask_b32_e64 v173, v2, v173, s[6:7]
	s_cmp_lg_u64 vcc, 0
	s_cselect_b32 s99, 1, 0
	v_mul_f32_e32 v2, 0xbe0293ee, v173
	v_fmamk_f32 v96, v96, 0x3e0293ee, v2
	v_fmamk_f32 v97, v97, 0x3e0293ee, v2
	v_fmamk_f32 v98, v98, 0x3e0293ee, v2
	v_fmamk_f32 v99, v99, 0x3e0293ee, v2
	v_fmamk_f32 v100, v100, 0x3e0293ee, v2
	v_fmamk_f32 v101, v101, 0x3e0293ee, v2
	v_fmamk_f32 v102, v102, 0x3e0293ee, v2
	v_fmamk_f32 v103, v103, 0x3e0293ee, v2
	v_fmamk_f32 v104, v104, 0x3e0293ee, v2
	v_fmamk_f32 v105, v105, 0x3e0293ee, v2
	v_fmamk_f32 v106, v106, 0x3e0293ee, v2
	v_fmamk_f32 v107, v107, 0x3e0293ee, v2
	v_fmamk_f32 v108, v108, 0x3e0293ee, v2
	v_fmamk_f32 v109, v109, 0x3e0293ee, v2
	v_fmamk_f32 v110, v110, 0x3e0293ee, v2
	v_fmamk_f32 v111, v111, 0x3e0293ee, v2
	v_exp_f32_e32 v96, v96
	v_fmamk_f32 v80, v80, 0x3e0293ee, v2
	v_exp_f32_e32 v97, v97
	v_fmamk_f32 v81, v81, 0x3e0293ee, v2
	v_exp_f32_e32 v98, v98
	v_fmamk_f32 v82, v82, 0x3e0293ee, v2
	v_exp_f32_e32 v99, v99
	v_fmamk_f32 v83, v83, 0x3e0293ee, v2
	v_exp_f32_e32 v100, v100
	v_fmamk_f32 v84, v84, 0x3e0293ee, v2
	v_exp_f32_e32 v101, v101
	v_fmamk_f32 v85, v85, 0x3e0293ee, v2
	v_exp_f32_e32 v102, v102
	v_fmamk_f32 v86, v86, 0x3e0293ee, v2
	v_exp_f32_e32 v103, v103
	v_fmamk_f32 v87, v87, 0x3e0293ee, v2
	v_exp_f32_e32 v104, v104
	v_fmamk_f32 v88, v88, 0x3e0293ee, v2
	v_exp_f32_e32 v105, v105
	v_fmamk_f32 v89, v89, 0x3e0293ee, v2
	v_exp_f32_e32 v106, v106
	v_fmamk_f32 v90, v90, 0x3e0293ee, v2
	v_exp_f32_e32 v107, v107
	v_fmamk_f32 v91, v91, 0x3e0293ee, v2
	v_exp_f32_e32 v108, v108
	v_fmamk_f32 v92, v92, 0x3e0293ee, v2
	v_exp_f32_e32 v109, v109
	v_fmamk_f32 v93, v93, 0x3e0293ee, v2
	v_exp_f32_e32 v110, v110
	v_fmamk_f32 v94, v94, 0x3e0293ee, v2
	v_exp_f32_e32 v111, v111
	v_fmamk_f32 v95, v95, 0x3e0293ee, v2
	s_add_i32 s6, s45, 2
	s_and_b32 s6, s6, 3
	s_lshl_b32 s6, s6, 8
	s_add_i32 s6, s6, 0x10800
	v_add_u32_e32 v152, s6, v164
	ds_read_b128 v[176:179], v152
	ds_read_b128 v[180:183], v152 offset:32
	ds_read_b128 v[192:195], v152 offset:128
	ds_read_b128 v[196:199], v152 offset:160
	ds_read_b128 v[184:187], v152 offset:64
	ds_read_b128 v[188:191], v152 offset:96
	ds_read_b128 v[200:203], v152 offset:192
	ds_read_b128 v[204:207], v152 offset:224
	s_branch .Lat_turn_end1
.Lat_steady1:
	s_waitcnt lgkmcnt(0)
	v_add3_u32 v246, v166, v165, s42
	v_add3_u32 v247, v168, v165, s42
	v_add3_u32 v248, v169, v165, s42
	v_add3_u32 v249, v170, v165, s42
	v_add_u32_e32 v153, s66, v162
	v_mfma_f32_32x32x16_bf16 v[96:111], v[208:211], v[112:115], v[96:111]
	ds_read_b128 v[208:211], v246 offset:128
	v_exp_f32_e32 v192, v192
	v_exp_f32_e32 v193, v193
	v_add_f32_e32 v148, v176, v180
	v_add_f32_e32 v149, v177, v181
	v_mfma_f32_32x32x16_bf16 v[80:95], v[212:215], v[112:115], v[80:95]
	ds_read_b128 v[212:215], v246 offset:8320
	v_exp_f32_e32 v194, v194
	v_exp_f32_e32 v195, v195
	v_add_f32_e32 v150, v178, v182
	v_add_f32_e32 v151, v179, v183
	v_mfma_f32_32x32x16_bf16 v[96:111], v[216:219], v[116:119], v[96:111]
	ds_read_b128 v[216:219], v247 offset:128
	v_exp_f32_e32 v196, v196
	v_exp_f32_e32 v197, v197
	v_add_f32_e32 v148, v148, v184
	v_add_f32_e32 v149, v149, v185
	v_mfma_f32_32x32x16_bf16 v[80:95], v[220:223], v[116:119], v[80:95]
	ds_read_b128 v[220:223], v247 offset:8320
	v_exp_f32_e32 v198, v198
	v_exp_f32_e32 v199, v199
	v_add_f32_e32 v150, v150, v186
	v_add_f32_e32 v151, v151, v187
	v_mfma_f32_32x32x16_bf16 v[96:111], v[224:227], v[120:123], v[96:111]
	ds_read_b128 v[224:227], v248 offset:128
	v_exp_f32_e32 v200, v200
	v_exp_f32_e32 v201, v201
	v_add_f32_e32 v148, v148, v188
	v_add_f32_e32 v149, v149, v189
	v_mfma_f32_32x32x16_bf16 v[80:95], v[234:237], v[120:123], v[80:95]
	ds_read_b128 v[234:237], v248 offset:8320
	v_exp_f32_e32 v202, v202
	v_exp_f32_e32 v203, v203
	v_add_f32_e32 v150, v150, v190
	v_add_f32_e32 v151, v151, v191
	v_mfma_f32_32x32x16_bf16 v[96:111], v[238:241], v[124:127], v[96:111]
	ds_read_b128 v[238:241], v249 offset:128
	v_exp_f32_e32 v204, v204
	v_exp_f32_e32 v205, v205
	v_add_f32_e32 v148, v148, v192
	v_add_f32_e32 v149, v149, v193
	v_mfma_f32_32x32x16_bf16 v[80:95], v[242:245], v[124:127], v[80:95]
	ds_read_b128 v[242:245], v249 offset:8320
	v_exp_f32_e32 v206, v206
	v_exp_f32_e32 v207, v207
	v_add_f32_e32 v150, v150, v194
	v_add_f32_e32 v151, v151, v195
	s_waitcnt lgkmcnt(7)
	v_mfma_f32_32x32x16_bf16 v[96:111], v[208:211], v[128:131], v[96:111]
	ds_read_b64_tr_b16 v[208:209], v153 offset:0
	ds_read_b64_tr_b16 v[210:211], v153 offset:2048
	v_add_f32_e32 v148, v148, v196
	v_add_f32_e32 v149, v149, v197
	v_add_f32_e32 v150, v150, v198
	v_add_f32_e32 v151, v151, v199
	v_add_f32_e32 v148, v148, v200
	v_add_f32_e32 v149, v149, v201
	s_waitcnt lgkmcnt(8)
	v_mfma_f32_32x32x16_bf16 v[80:95], v[212:215], v[128:131], v[80:95]
	ds_read_b64_tr_b16 v[212:213], v153 offset:512
	ds_read_b64_tr_b16 v[214:215], v153 offset:2560
	v_add_f32_e32 v150, v150, v202
	v_add_f32_e32 v151, v151, v203
	v_add_f32_e32 v148, v148, v204
	v_add_f32_e32 v149, v149, v205
	v_add_f32_e32 v150, v150, v206
	v_add_f32_e32 v151, v151, v207
	s_waitcnt lgkmcnt(9)
	v_mfma_f32_32x32x16_bf16 v[96:111], v[216:219], v[132:135], v[96:111]
	ds_read_b64_tr_b16 v[216:217], v153 offset:1024
	ds_read_b64_tr_b16 v[218:219], v153 offset:3072
	v_add_f32_e32 v148, v148, v149
	v_add_f32_e32 v150, v150, v151
	v_add_f32_e32 v148, v148, v150
	v_mov_b32_e32 v152, v148
	v_cvt_pk_bf16_f32 v176, v176, v177
	v_cvt_pk_bf16_f32 v177, v178, v179
	s_waitcnt lgkmcnt(10)
	v_mfma_f32_32x32x16_bf16 v[80:95], v[220:223], v[132:135], v[80:95]
	ds_read_b64_tr_b16 v[220:221], v153 offset:1536
	ds_read_b64_tr_b16 v[222:223], v153 offset:3584
	v_permlane32_swap_b32_e32 v148, v152
	v_cvt_pk_bf16_f32 v178, v180, v181
	v_cvt_pk_bf16_f32 v179, v182, v183
	v_add_f32_e32 v148, v148, v152
	v_cvt_pk_bf16_f32 v180, v184, v185
	v_cvt_pk_bf16_f32 v181, v186, v187
	s_waitcnt lgkmcnt(11)
	v_mfma_f32_32x32x16_bf16 v[96:111], v[224:227], v[136:139], v[96:111]
	ds_read_b64_tr_b16 v[224:225], v153 offset:4096
	ds_read_b64_tr_b16 v[226:227], v153 offset:6144
	v_cvt_pk_bf16_f32 v182, v188, v189
	v_cvt_pk_bf16_f32 v183, v190, v191
	v_cvt_pk_bf16_f32 v184, v192, v193
	v_cvt_pk_bf16_f32 v185, v194, v195
	v_cvt_pk_bf16_f32 v186, v196, v197
	v_cvt_pk_bf16_f32 v187, v198, v199
	s_waitcnt lgkmcnt(12)
	v_mfma_f32_32x32x16_bf16 v[80:95], v[234:237], v[136:139], v[80:95]
	ds_read_b64_tr_b16 v[234:235], v153 offset:4608
	ds_read_b64_tr_b16 v[236:237], v153 offset:6656
	v_cvt_pk_bf16_f32 v188, v200, v201
	v_cvt_pk_bf16_f32 v189, v202, v203
	v_cvt_pk_bf16_f32 v190, v204, v205
	v_cvt_pk_bf16_f32 v191, v206, v207
	v_fma_f32 v174, v174, v233, v148
	s_nop 0
	s_waitcnt lgkmcnt(13)
	v_mfma_f32_32x32x16_bf16 v[96:111], v[238:241], v[140:143], v[96:111]
	ds_read_b64_tr_b16 v[238:239], v153 offset:5120
	ds_read_b64_tr_b16 v[240:241], v153 offset:7168
	v_permlane32_swap_b32_e32 v176, v178
	v_permlane32_swap_b32_e32 v177, v179
	v_permlane32_swap_b32_e32 v180, v182
	v_permlane32_swap_b32_e32 v181, v183
	v_permlane32_swap_b32_e32 v184, v186
	v_permlane32_swap_b32_e32 v185, v187
	s_waitcnt lgkmcnt(14)
	v_mfma_f32_32x32x16_bf16 v[80:95], v[242:245], v[140:143], v[80:95]
	ds_read_b64_tr_b16 v[242:243], v153 offset:5632
	ds_read_b64_tr_b16 v[244:245], v153 offset:7680
	v_permlane32_swap_b32_e32 v188, v190
	v_permlane32_swap_b32_e32 v189, v191
	s_add_i32 s6, s65, -1
	s_cmp_gt_i32 s6, s44
	s_cbranch_scc1 .Lat_mask1
	s_cmp_lt_i32 s65, 0xb0
	s_cbranch_scc0 .Lat_nomask1

.Lat_norescale1:
	v_add3_u32 v246, v166, v165, s43
	v_add3_u32 v247, v168, v165, s43
	v_add3_u32 v248, v169, v165, s43
	v_add3_u32 v249, v170, v165, s43
	s_add_i32 s6, s45, 2
	s_and_b32 s6, s6, 3
	s_lshl_b32 s6, s6, 8
	s_add_i32 s6, s6, 0x10800
	v_add_u32_e32 v152, s6, v164
	s_add_i32 s6, s45, 1
	s_cmp_ge_u32 s6, s46
	s_cbranch_scc1 .Lat_p2last1
	s_waitcnt lgkmcnt(14)
	v_mfma_f32_32x32x16_bf16 v[64:79], v[176:179], v[208:211], v[64:79]
	ds_read_b64_tr_b16 v[208:209], v153 offset:8192
	ds_read_b64_tr_b16 v[210:211], v153 offset:10240
	ds_read_b128 v[192:195], v152 offset:128
	s_waitcnt lgkmcnt(15)
	v_mfma_f32_32x32x16_bf16 v[48:63], v[176:179], v[212:215], v[48:63]
	ds_read_b64_tr_b16 v[212:213], v153 offset:8704
	ds_read_b64_tr_b16 v[214:215], v153 offset:10752
	ds_read_b128 v[196:199], v152 offset:160
	v_max3_f32 v0, v96, v97, v98
	v_max3_f32 v2, v104, v105, v106
	v_max3_f32 v3, v80, v81, v82
	v_max3_f32 v4, v88, v89, v90
	v_max3_f32 v0, v0, v99, v100
	v_max3_f32 v2, v2, v107, v108
	s_waitcnt lgkmcnt(15)
	v_mfma_f32_32x32x16_bf16 v[32:47], v[176:179], v[216:219], v[32:47]
	ds_read_b64_tr_b16 v[216:217], v153 offset:9216
	ds_read_b64_tr_b16 v[218:219], v153 offset:11264
	ds_read_b128 v[200:203], v152 offset:192
	v_max3_f32 v3, v3, v83, v84
	v_max3_f32 v4, v4, v91, v92
	v_max3_f32 v0, v0, v101, v102
	v_max3_f32 v2, v2, v109, v110
	v_max3_f32 v3, v3, v85, v86
	v_max3_f32 v4, v4, v93, v94
	s_waitcnt lgkmcnt(15)
	v_mfma_f32_32x32x16_bf16 v[16:31], v[176:179], v[220:223], v[16:31]
	ds_read_b64_tr_b16 v[220:221], v153 offset:9728
	ds_read_b64_tr_b16 v[222:223], v153 offset:11776
	ds_read_b128 v[204:207], v152 offset:224
	ds_read_b128 v[176:179], v152
	v_max_f32_e32 v0, v0, v103
	v_max_f32_e32 v2, v2, v111
	v_max_f32_e32 v3, v3, v87
	v_max_f32_e32 v4, v4, v95
	v_max3_f32 v0, v0, v2, v3
	v_max_f32_e32 v0, v0, v4
	s_waitcnt lgkmcnt(15)
	v_mfma_f32_32x32x16_bf16 v[64:79], v[180:183], v[224:227], v[64:79]
	ds_read_b64_tr_b16 v[224:225], v153 offset:12288
	ds_read_b64_tr_b16 v[226:227], v153 offset:14336
	v_mov_b32_e32 v2, v0
	s_nop 1
	v_permlane32_swap_b32_e32 v0, v2
	v_max_f32_e32 v2, v2, v2
	v_max_f32_e32 v0, v0, v0
	s_waitcnt lgkmcnt(15)
	v_mfma_f32_32x32x16_bf16 v[48:63], v[180:183], v[234:237], v[48:63]
	ds_read_b64_tr_b16 v[234:235], v153 offset:12800
	ds_read_b64_tr_b16 v[236:237], v153 offset:14848
	v_max_f32_e32 v0, v0, v2
	v_sub_f32_e32 v2, v0, v173
	v_mul_f32_e32 v2, 0x3db504f3, v2
	v_cmp_ge_f32_e32 vcc, s63, v2
	v_max_f32_e32 v2, v173, v173
	v_max_f32_e32 v2, v2, v0
	s_waitcnt lgkmcnt(15)
	v_mfma_f32_32x32x16_bf16 v[32:47], v[180:183], v[238:241], v[32:47]
	ds_read_b64_tr_b16 v[238:239], v153 offset:13312
	ds_read_b64_tr_b16 v[240:241], v153 offset:15360
	v_sub_f32_e32 v0, v173, v2
	v_mul_f32_e32 v0, 0x3e0293ee, v0
	v_exp_f32_e32 v0, v0
	s_cmp_eq_u64 vcc, exec
	s_cselect_b64 s[6:7], -1, 0
	v_cndmask_b32_e64 v0, v0, 1.0, s[6:7]
	s_waitcnt lgkmcnt(15)
	v_mfma_f32_32x32x16_bf16 v[16:31], v[180:183], v[242:245], v[16:31]
	ds_read_b64_tr_b16 v[242:243], v153 offset:13824
	ds_read_b64_tr_b16 v[244:245], v153 offset:15872
	ds_read_b128 v[180:183], v152 offset:32
	v_cmp_gt_f32_e32 vcc, 1.0, v0
	v_mov_b32_e32 v233, v0
	v_cndmask_b32_e64 v173, v2, v173, s[6:7]
	s_cmp_lg_u64 vcc, 0
	s_cselect_b32 s99, 1, 0
	v_mul_f32_e32 v2, 0xbe0293ee, v173
	v_fmamk_f32 v96, v96, 0x3e0293ee, v2
	s_waitcnt lgkmcnt(15)
	v_mfma_f32_32x32x16_bf16 v[64:79], v[184:187], v[208:211], v[64:79]
	ds_read_b128 v[208:211], v246
	v_fmamk_f32 v97, v97, 0x3e0293ee, v2
	v_fmamk_f32 v98, v98, 0x3e0293ee, v2
	v_fmamk_f32 v99, v99, 0x3e0293ee, v2
	v_fmamk_f32 v100, v100, 0x3e0293ee, v2
	v_fmamk_f32 v101, v101, 0x3e0293ee, v2
	v_fmamk_f32 v102, v102, 0x3e0293ee, v2
	s_waitcnt lgkmcnt(15)
	v_mfma_f32_32x32x16_bf16 v[48:63], v[184:187], v[212:215], v[48:63]
	ds_read_b128 v[212:215], v246 offset:8192
	v_fmamk_f32 v103, v103, 0x3e0293ee, v2
	v_fmamk_f32 v104, v104, 0x3e0293ee, v2
	v_fmamk_f32 v105, v105, 0x3e0293ee, v2
	v_fmamk_f32 v106, v106, 0x3e0293ee, v2
	v_fmamk_f32 v107, v107, 0x3e0293ee, v2
	v_fmamk_f32 v108, v108, 0x3e0293ee, v2
	s_waitcnt lgkmcnt(15)
	v_mfma_f32_32x32x16_bf16 v[32:47], v[184:187], v[216:219], v[32:47]
	ds_read_b128 v[216:219], v247
	v_fmamk_f32 v109, v109, 0x3e0293ee, v2
	v_fmamk_f32 v110, v110, 0x3e0293ee, v2
	v_fmamk_f32 v111, v111, 0x3e0293ee, v2
	v_exp_f32_e32 v96, v96
	v_fmamk_f32 v80, v80, 0x3e0293ee, v2
	s_waitcnt lgkmcnt(14)
	v_mfma_f32_32x32x16_bf16 v[16:31], v[184:187], v[220:223], v[16:31]
	ds_read_b128 v[220:223], v247 offset:8192
	ds_read_b128 v[184:187], v152 offset:64
	v_exp_f32_e32 v97, v97
	v_fmamk_f32 v81, v81, 0x3e0293ee, v2
	v_exp_f32_e32 v98, v98
	v_fmamk_f32 v82, v82, 0x3e0293ee, v2
	s_waitcnt lgkmcnt(12)
	v_mfma_f32_32x32x16_bf16 v[64:79], v[188:191], v[224:227], v[64:79]
	ds_read_b128 v[224:227], v248
	v_exp_f32_e32 v99, v99
	v_fmamk_f32 v83, v83, 0x3e0293ee, v2
	v_exp_f32_e32 v100, v100
	v_fmamk_f32 v84, v84, 0x3e0293ee, v2
	s_waitcnt lgkmcnt(11)
	v_mfma_f32_32x32x16_bf16 v[48:63], v[188:191], v[234:237], v[48:63]
	ds_read_b128 v[234:237], v248 offset:8192
	v_exp_f32_e32 v101, v101
	v_fmamk_f32 v85, v85, 0x3e0293ee, v2
	v_exp_f32_e32 v102, v102
	v_fmamk_f32 v86, v86, 0x3e0293ee, v2
	s_waitcnt lgkmcnt(10)
	v_mfma_f32_32x32x16_bf16 v[32:47], v[188:191], v[238:241], v[32:47]
	ds_read_b128 v[238:241], v249
	v_exp_f32_e32 v103, v103
	v_fmamk_f32 v87, v87, 0x3e0293ee, v2
	v_exp_f32_e32 v104, v104
	v_fmamk_f32 v88, v88, 0x3e0293ee, v2
	s_waitcnt lgkmcnt(9)
	v_mfma_f32_32x32x16_bf16 v[16:31], v[188:191], v[242:245], v[16:31]
	ds_read_b128 v[242:245], v249 offset:8192
	ds_read_b128 v[188:191], v152 offset:96
	v_exp_f32_e32 v105, v105
	v_fmamk_f32 v89, v89, 0x3e0293ee, v2
	v_exp_f32_e32 v106, v106
	v_fmamk_f32 v90, v90, 0x3e0293ee, v2
	v_exp_f32_e32 v107, v107
	v_fmamk_f32 v91, v91, 0x3e0293ee, v2
	v_exp_f32_e32 v108, v108
	v_fmamk_f32 v92, v92, 0x3e0293ee, v2
	v_exp_f32_e32 v109, v109
	v_fmamk_f32 v93, v93, 0x3e0293ee, v2
	v_exp_f32_e32 v110, v110
	v_fmamk_f32 v94, v94, 0x3e0293ee, v2
	v_exp_f32_e32 v111, v111
	v_fmamk_f32 v95, v95, 0x3e0293ee, v2
	s_branch .Lat_turn_end1
.Lat_p2last1:
	s_waitcnt lgkmcnt(14)
	v_mfma_f32_32x32x16_bf16 v[64:79], v[176:179], v[208:211], v[64:79]
	ds_read_b64_tr_b16 v[208:209], v153 offset:8192
	ds_read_b64_tr_b16 v[210:211], v153 offset:10240
	ds_read_b128 v[192:195], v152 offset:128
	s_waitcnt lgkmcnt(15)
	v_mfma_f32_32x32x16_bf16 v[48:63], v[176:179], v[212:215], v[48:63]
	ds_read_b64_tr_b16 v[212:213], v153 offset:8704
	ds_read_b64_tr_b16 v[214:215], v153 offset:10752
	ds_read_b128 v[196:199], v152 offset:160
	s_waitcnt lgkmcnt(15)
	v_mfma_f32_32x32x16_bf16 v[32:47], v[176:179], v[216:219], v[32:47]
	ds_read_b64_tr_b16 v[216:217], v153 offset:9216
	ds_read_b64_tr_b16 v[218:219], v153 offset:11264
	ds_read_b128 v[200:203], v152 offset:192
	s_waitcnt lgkmcnt(15)
	v_mfma_f32_32x32x16_bf16 v[16:31], v[176:179], v[220:223], v[16:31]
	ds_read_b64_tr_b16 v[220:221], v153 offset:9728
	ds_read_b64_tr_b16 v[222:223], v153 offset:11776
	ds_read_b128 v[204:207], v152 offset:224
	ds_read_b128 v[176:179], v152
	s_waitcnt lgkmcnt(15)
	v_mfma_f32_32x32x16_bf16 v[64:79], v[180:183], v[224:227], v[64:79]
	ds_read_b64_tr_b16 v[224:225], v153 offset:12288
	ds_read_b64_tr_b16 v[226:227], v153 offset:14336
	s_waitcnt lgkmcnt(15)
	v_mfma_f32_32x32x16_bf16 v[48:63], v[180:183], v[234:237], v[48:63]
	ds_read_b64_tr_b16 v[234:235], v153 offset:12800
	ds_read_b64_tr_b16 v[236:237], v153 offset:14848
	s_waitcnt lgkmcnt(15)
	v_mfma_f32_32x32x16_bf16 v[32:47], v[180:183], v[238:241], v[32:47]
	ds_read_b64_tr_b16 v[238:239], v153 offset:13312
	ds_read_b64_tr_b16 v[240:241], v153 offset:15360
	s_waitcnt lgkmcnt(15)
	v_mfma_f32_32x32x16_bf16 v[16:31], v[180:183], v[242:245], v[16:31]
	ds_read_b64_tr_b16 v[242:243], v153 offset:13824
	ds_read_b64_tr_b16 v[244:245], v153 offset:15872
	ds_read_b128 v[180:183], v152 offset:32
	s_waitcnt lgkmcnt(15)
	v_mfma_f32_32x32x16_bf16 v[64:79], v[184:187], v[208:211], v[64:79]
	ds_read_b128 v[208:211], v246
	s_waitcnt lgkmcnt(15)
	v_mfma_f32_32x32x16_bf16 v[48:63], v[184:187], v[212:215], v[48:63]
	ds_read_b128 v[212:215], v246 offset:8192
	s_waitcnt lgkmcnt(15)
	v_mfma_f32_32x32x16_bf16 v[32:47], v[184:187], v[216:219], v[32:47]
	ds_read_b128 v[216:219], v247
	s_waitcnt lgkmcnt(14)
	v_mfma_f32_32x32x16_bf16 v[16:31], v[184:187], v[220:223], v[16:31]
	ds_read_b128 v[220:223], v247 offset:8192
	ds_read_b128 v[184:187], v152 offset:64
	s_waitcnt lgkmcnt(12)
	v_mfma_f32_32x32x16_bf16 v[64:79], v[188:191], v[224:227], v[64:79]
	ds_read_b128 v[224:227], v248
	s_waitcnt lgkmcnt(11)
	v_mfma_f32_32x32x16_bf16 v[48:63], v[188:191], v[234:237], v[48:63]
	ds_read_b128 v[234:237], v248 offset:8192
	s_waitcnt lgkmcnt(10)
	v_mfma_f32_32x32x16_bf16 v[32:47], v[188:191], v[238:241], v[32:47]
	ds_read_b128 v[238:241], v249
	s_waitcnt lgkmcnt(9)
	v_mfma_f32_32x32x16_bf16 v[16:31], v[188:191], v[242:245], v[16:31]
	ds_read_b128 v[242:245], v249 offset:8192
	ds_read_b128 v[188:191], v152 offset:96

.Lat_wd1:
	s_cmp_lg_u32 s68, 0x2000
	s_cbranch_scc1 .Lat_next1
	s_add_i32 s6, s45, 2
	s_cmp_ge_u32 s6, s46
	s_cbranch_scc1 .Lat_next1
	s_cmp_lt_u32 s45, 1
	s_cbranch_scc1 .Lat_next1
	s_and_b32 s7, s6, 3
	s_lshl_b32 s7, s7, 8
	v_add_u32_e32 v0, s7, v171
	ds_write_b32 v0, v172
.Lat_next1:
	s_cmp_lt_u32 s45, s46
	s_cbranch_scc1 .Lat_tile0
.Lat_done:
	s_waitcnt lgkmcnt(0)
	s_waitcnt vmcnt(0)
